# static priority: per-cluster s_setprio flips deleted in the five GEMM loops, one raise for waves 4-7 per phase
# speedup vs baseline: 1.0096x; 1.0096x over previous
; template <class Epi, class Sched, bool FP8 = false>
; __device__ __forceinline__ void gemm_phase(LAS unsigned char* lds, const int K, const Sched& S, const Epi& E) {
;     ...
;     const int tid = threadIdx.x, wid = __builtin_amdgcn_readfirstlane(tid >> 6), lane = tid & 63, wr = wid >> 2, wc = wid & 3, fr = lane & 15, fq = lane >> 4;
; __global__ void __launch_bounds__(512, 2) fwd(Args args) {
;     ...
;     if (IN(2)) { { PH_IDS
;         InSched S; S.D.init(ws + RA_H, ws + WS_WIN, 2048, 2048, NT, G == 256 ? 15 * 256 : DINP, G, bx); S.done = (unsigned*)(ws + WS_CTL) + CTL_INPROJ_DONE;
;         EpiIn E{ws};
;         pg8::gemm_phase<EpiIn, InSched>(lds, 2048, S, E); }
.LBB0_143:
	v_readfirstlane_b32 s0, v0
	s_nop 3
	s_lshr_b32 s0, s0, 6
	s_cmp_ge_u32 s0, 4
	s_cbranch_scc0 .Lprio_p2
	s_setprio 1

; #define PG8_STAGE(bufoff, gbase, v0, v1) do { \
;         __builtin_amdgcn_global_load_lds((const unsigned*)((const char*)(gbase) + (v0)), (LAS unsigned*)(lds + (bufoff) + ldsw), 16, 0, 0); \
;         __builtin_amdgcn_global_load_lds((const unsigned*)((const char*)(gbase) + (v1)), (LAS unsigned*)(lds + (bufoff) + ldsw + 8192), 16, 0, 0); } while (0)
; #define PG8_LDA(dst, b, h) do { _Pragma("unroll") for (int m = 0; m < 4; ++m) { const v4i lo_ = *(const LAS v4i*)(lds + PG8_SA(b, h) + aoff + m * 2048), hi_ = *(const LAS v4i*)(lds + PG8_SA(b, h) + aoff + m * 2048 + 1024); \
;         dst[m] = __builtin_shufflevector(lo_, hi_, 0, 1, 2, 3, 4, 5, 6, 7); } } while (0)
; #define PG8_LDB(dst, b, h) do { _Pragma("unroll") for (int n = 0; n < 2; ++n) { const v4i lo_ = *(const LAS v4i*)(lds + PG8_SB(b, h) + boff + n * 2048), hi_ = *(const LAS v4i*)(lds + PG8_SB(b, h) + boff + n * 2048 + 1024); \
;         dst[n] = __builtin_shufflevector(lo_, hi_, 0, 1, 2, 3, 4, 5, 6, 7); } } while (0)
; #define PG8_WAIT_V(n) asm volatile("s_waitcnt vmcnt(" #n ")" ::: "memory")
; #define PG8_WAIT_L(n) asm volatile("s_waitcnt lgkmcnt(" #n ")" ::: "memory")
; #define PG8_BAR __builtin_amdgcn_s_barrier()
; #define PG8_SCHED __builtin_amdgcn_sched_barrier(0)
; template <class Epi, class Sched, bool FP8 = false>
; __device__ __forceinline__ void gemm_phase(LAS unsigned char* lds, const int K, const Sched& S, const Epi& E) {
;     ...
;             PG8_LDB(B0, 0, 0); PG8_LDB(B1, 0, 1); PG8_SCHED; PG8_LDA(At, 0, 0); PG8_STAGE(PG8_SA(1, 1), a1, vA[2], vA[3]);
;             PG8_WAIT_V(8); PG8_WAIT_L(0); PG8_BAR; PG8_MMA(0, 0, At, B0); PG8_MMA(0, 1, At, B1); PG8_BAR; PG8_SCHED;
;             PG8_LDA(At, 0, 1); PG8_STAGE(PG8_SB(0, 0), b2, voffB[0], voffB[1]); PG8_STAGE(PG8_SB(0, 1), b2 + hstepB, voffB[0], voffB[1]); PG8_STAGE(PG8_SA(0, 0), a2, x0, x1);
;             PG8_WAIT_V(8); PG8_WAIT_L(0); PG8_BAR; if (!lo_only) { PG8_MMA(1, 0, At, B0); PG8_MMA(1, 1, At, B1); } PG8_BAR; PG8_SCHED;
.LBB0_209:
	v_add_u32_e32 v142, s51, v1
	ds_read_b128 v[154:157], v142
	ds_read_b128 v[158:161], v142 offset:1024
	ds_read_b128 v[162:165], v142 offset:2048
	ds_read_b128 v[166:169], v142 offset:3072
	v_add_u32_e32 v142, s73, v1
	s_add_u32 s34, s10, s70
	ds_read_b128 v[170:173], v142
	ds_read_b128 v[174:177], v142 offset:1024
	ds_read_b128 v[178:181], v142 offset:2048
	ds_read_b128 v[182:185], v142 offset:3072
	s_addc_u32 s35, s11, s71
	s_add_u32 s34, s34, 0x100
	s_addc_u32 s35, s35, 0
	s_add_u32 s80, s9, s70
	s_addc_u32 s81, s14, s71
	s_cmpk_eq_i32 s70, 0xf00
	s_cselect_b32 s35, s2, s35
	s_cselect_b32 s34, s3, s34
	s_cselect_b32 s81, s25, s81
	s_cselect_b32 s80, s96, s80
	v_lshl_add_u64 v[218:219], v[148:149], 0, s[70:71]
	s_add_i32 m0, s39, 0xc000
	ds_read_b128 v[186:189], v152
	ds_read_b128 v[190:193], v152 offset:1024
	ds_read_b128 v[194:197], v152 offset:2048
	ds_read_b128 v[198:201], v152 offset:3072
	ds_read_b128 v[202:205], v152 offset:4096
	ds_read_b128 v[206:209], v152 offset:5120
	ds_read_b128 v[210:213], v152 offset:6144
	ds_read_b128 v[214:217], v152 offset:7168
	global_load_lds_dwordx4 v[218:219], off
	v_lshl_add_u64 v[218:219], v[150:151], 0, s[70:71]
	s_add_i32 m0, s39, 0xe000
	s_nop 0
	global_load_lds_dwordx4 v[218:219], off
	s_waitcnt vmcnt(8)
	s_waitcnt lgkmcnt(0)
	s_barrier
	s_waitcnt lgkmcnt(0)
	v_mfma_f32_16x16x32_bf16 v[126:129], v[154:157], v[186:189], v[126:129]
	v_mfma_f32_16x16x32_bf16 v[122:125], v[162:165], v[186:189], v[122:125]
	v_mfma_f32_16x16x32_bf16 v[118:121], v[154:157], v[194:197], v[118:121]
	v_mfma_f32_16x16x32_bf16 v[114:117], v[162:165], v[194:197], v[114:117]
	v_mfma_f32_16x16x32_bf16 v[110:113], v[154:157], v[202:205], v[110:113]
	v_mfma_f32_16x16x32_bf16 v[106:109], v[162:165], v[202:205], v[106:109]
	v_mfma_f32_16x16x32_bf16 v[102:105], v[154:157], v[210:213], v[102:105]
	v_mfma_f32_16x16x32_bf16 v[98:101], v[162:165], v[210:213], v[98:101]
	v_mfma_f32_16x16x32_bf16 v[126:129], v[158:161], v[190:193], v[126:129]
	v_mfma_f32_16x16x32_bf16 v[122:125], v[166:169], v[190:193], v[122:125]
	v_mfma_f32_16x16x32_bf16 v[118:121], v[158:161], v[198:201], v[118:121]
	v_mfma_f32_16x16x32_bf16 v[114:117], v[166:169], v[198:201], v[114:117]
	v_mfma_f32_16x16x32_bf16 v[110:113], v[158:161], v[206:209], v[110:113]
	v_mfma_f32_16x16x32_bf16 v[106:109], v[166:169], v[206:209], v[106:109]
	v_mfma_f32_16x16x32_bf16 v[102:105], v[158:161], v[214:217], v[102:105]
	v_mfma_f32_16x16x32_bf16 v[98:101], v[166:169], v[214:217], v[98:101]
	v_mfma_f32_16x16x32_bf16 v[94:97], v[170:173], v[186:189], v[94:97]
	v_mfma_f32_16x16x32_bf16 v[90:93], v[178:181], v[186:189], v[90:93]
	v_mfma_f32_16x16x32_bf16 v[86:89], v[170:173], v[194:197], v[86:89]
	v_mfma_f32_16x16x32_bf16 v[82:85], v[178:181], v[194:197], v[82:85]
	v_mfma_f32_16x16x32_bf16 v[78:81], v[170:173], v[202:205], v[78:81]
	v_mfma_f32_16x16x32_bf16 v[74:77], v[178:181], v[202:205], v[74:77]
	v_mfma_f32_16x16x32_bf16 v[70:73], v[170:173], v[210:213], v[70:73]
	v_mfma_f32_16x16x32_bf16 v[66:69], v[178:181], v[210:213], v[66:69]
	v_mfma_f32_16x16x32_bf16 v[94:97], v[174:177], v[190:193], v[94:97]
	v_mfma_f32_16x16x32_bf16 v[90:93], v[182:185], v[190:193], v[90:93]
	v_mfma_f32_16x16x32_bf16 v[86:89], v[174:177], v[198:201], v[86:89]
	v_mfma_f32_16x16x32_bf16 v[82:85], v[182:185], v[198:201], v[82:85]
	v_mfma_f32_16x16x32_bf16 v[78:81], v[174:177], v[206:209], v[78:81]
	v_mfma_f32_16x16x32_bf16 v[74:77], v[182:185], v[206:209], v[74:77]
	v_mfma_f32_16x16x32_bf16 v[70:73], v[174:177], v[214:217], v[70:73]
	v_mfma_f32_16x16x32_bf16 v[66:69], v[182:185], v[214:217], v[66:69]
	s_barrier
	s_add_i32 vcc_lo, s51, s13
	v_lshl_add_u64 v[218:219], s[80:81], 0, v[130:131]
	s_mov_b32 m0, vcc_lo
	ds_read_b128 v[186:189], v152 offset:16384
	ds_read_b128 v[190:193], v152 offset:17408
	ds_read_b128 v[194:197], v152 offset:18432
	ds_read_b128 v[198:201], v152 offset:19456
	ds_read_b128 v[202:205], v152 offset:20480
	ds_read_b128 v[206:209], v152 offset:21504
	ds_read_b128 v[210:213], v152 offset:22528
	ds_read_b128 v[214:217], v152 offset:23552
	global_load_lds_dwordx4 v[218:219], off
	s_add_i32 m0, vcc_lo, 0x2000
	s_add_u32 vcc_lo, s80, 0x80000
	v_lshl_add_u64 v[220:221], s[80:81], 0, v[132:133]
	s_addc_u32 vcc_hi, s81, 0
	s_add_i32 s48, s73, s13
	global_load_lds_dwordx4 v[220:221], off
	v_lshl_add_u64 v[222:223], vcc, 0, v[130:131]
	s_mov_b32 m0, s48
	v_lshl_add_u64 v[224:225], s[34:35], 0, v[136:137]
	global_load_lds_dwordx4 v[222:223], off
	v_lshl_add_u64 v[222:223], vcc, 0, v[132:133]
	s_add_i32 m0, s48, 0x2000
	s_nop 0
	global_load_lds_dwordx4 v[222:223], off
	v_lshl_add_u64 v[222:223], s[34:35], 0, v[134:135]
	s_mov_b32 m0, s39
	s_nop 0
	global_load_lds_dwordx4 v[222:223], off
	s_mov_b32 m0, s40
	s_nop 0
	global_load_lds_dwordx4 v[224:225], off
	s_waitcnt vmcnt(8)
	s_waitcnt lgkmcnt(0)
	s_barrier
; #define PG8_STAGE(bufoff, gbase, v0, v1) do { \
;         __builtin_amdgcn_global_load_lds((const unsigned*)((const char*)(gbase) + (v0)), (LAS unsigned*)(lds + (bufoff) + ldsw), 16, 0, 0); \
;         __builtin_amdgcn_global_load_lds((const unsigned*)((const char*)(gbase) + (v1)), (LAS unsigned*)(lds + (bufoff) + ldsw + 8192), 16, 0, 0); } while (0)
; #define PG8_LDA(dst, b, h) do { _Pragma("unroll") for (int m = 0; m < 4; ++m) { const v4i lo_ = *(const LAS v4i*)(lds + PG8_SA(b, h) + aoff + m * 2048), hi_ = *(const LAS v4i*)(lds + PG8_SA(b, h) + aoff + m * 2048 + 1024); \
;         dst[m] = __builtin_shufflevector(lo_, hi_, 0, 1, 2, 3, 4, 5, 6, 7); } } while (0)
; #define PG8_LDB(dst, b, h) do { _Pragma("unroll") for (int n = 0; n < 2; ++n) { const v4i lo_ = *(const LAS v4i*)(lds + PG8_SB(b, h) + boff + n * 2048), hi_ = *(const LAS v4i*)(lds + PG8_SB(b, h) + boff + n * 2048 + 1024); \
;         dst[n] = __builtin_shufflevector(lo_, hi_, 0, 1, 2, 3, 4, 5, 6, 7); } } while (0)
; #define PG8_WAIT_V(n) asm volatile("s_waitcnt vmcnt(" #n ")" ::: "memory")
; #define PG8_WAIT_L(n) asm volatile("s_waitcnt lgkmcnt(" #n ")" ::: "memory")
; #define PG8_BAR __builtin_amdgcn_s_barrier()
; #define PG8_SCHED __builtin_amdgcn_sched_barrier(0)
; template <class Epi, class Sched, bool FP8 = false>
; __device__ __forceinline__ void gemm_phase(LAS unsigned char* lds, const int K, const Sched& S, const Epi& E) {
;     ...
;             PG8_WAIT_V(8); PG8_WAIT_L(0); PG8_BAR; if (!lo_only) { PG8_MMA(1, 0, At, B0); PG8_MMA(1, 1, At, B1); } PG8_BAR; PG8_SCHED;
;             PG8_LDB(B0, 1, 0); PG8_LDB(B1, 1, 1); PG8_SCHED; PG8_LDA(At, 1, 0); PG8_STAGE(PG8_SA(0, 1), a2, x2, x3);
;             PG8_WAIT_V(8); PG8_WAIT_L(0); PG8_BAR; PG8_MMA(0, 0, At, B0); PG8_MMA(0, 1, At, B1); PG8_BAR; PG8_SCHED;
;             PG8_LDA(At, 1, 1); PG8_STAGE(PG8_SB(1, 0), b3, voffB[0], voffB[1]); PG8_STAGE(PG8_SB(1, 1), b3 + hstepB, voffB[0], voffB[1]); PG8_STAGE(PG8_SA(1, 0), a3, x0, x1);
	s_waitcnt lgkmcnt(0)
	v_mfma_f32_16x16x32_bf16 v[62:65], v[154:157], v[186:189], v[62:65]
	v_mfma_f32_16x16x32_bf16 v[58:61], v[162:165], v[186:189], v[58:61]
	v_mfma_f32_16x16x32_bf16 v[54:57], v[154:157], v[194:197], v[54:57]
	v_mfma_f32_16x16x32_bf16 v[50:53], v[162:165], v[194:197], v[50:53]
	v_mfma_f32_16x16x32_bf16 v[46:49], v[154:157], v[202:205], v[46:49]
	v_mfma_f32_16x16x32_bf16 v[42:45], v[162:165], v[202:205], v[42:45]
	v_mfma_f32_16x16x32_bf16 v[38:41], v[154:157], v[210:213], v[38:41]
	v_mfma_f32_16x16x32_bf16 v[34:37], v[162:165], v[210:213], v[34:37]
	v_mfma_f32_16x16x32_bf16 v[62:65], v[158:161], v[190:193], v[62:65]
	v_mfma_f32_16x16x32_bf16 v[58:61], v[166:169], v[190:193], v[58:61]
	v_mfma_f32_16x16x32_bf16 v[54:57], v[158:161], v[198:201], v[54:57]
	v_mfma_f32_16x16x32_bf16 v[50:53], v[166:169], v[198:201], v[50:53]
	v_mfma_f32_16x16x32_bf16 v[46:49], v[158:161], v[206:209], v[46:49]
	v_mfma_f32_16x16x32_bf16 v[42:45], v[166:169], v[206:209], v[42:45]
	v_mfma_f32_16x16x32_bf16 v[38:41], v[158:161], v[214:217], v[38:41]
	v_mfma_f32_16x16x32_bf16 v[34:37], v[166:169], v[214:217], v[34:37]
	v_mfma_f32_16x16x32_bf16 v[30:33], v[170:173], v[186:189], v[30:33]
	v_mfma_f32_16x16x32_bf16 v[26:29], v[178:181], v[186:189], v[26:29]
	v_mfma_f32_16x16x32_bf16 v[22:25], v[170:173], v[194:197], v[22:25]
	v_mfma_f32_16x16x32_bf16 v[18:21], v[178:181], v[194:197], v[18:21]
	v_mfma_f32_16x16x32_bf16 v[14:17], v[170:173], v[202:205], v[14:17]
	v_mfma_f32_16x16x32_bf16 v[10:13], v[178:181], v[202:205], v[10:13]
	v_mfma_f32_16x16x32_bf16 v[6:9], v[170:173], v[210:213], v[6:9]
	v_mfma_f32_16x16x32_bf16 v[2:5], v[178:181], v[210:213], v[2:5]
	v_mfma_f32_16x16x32_bf16 v[30:33], v[174:177], v[190:193], v[30:33]
	v_mfma_f32_16x16x32_bf16 v[26:29], v[182:185], v[190:193], v[26:29]
	v_mfma_f32_16x16x32_bf16 v[22:25], v[174:177], v[198:201], v[22:25]
	v_mfma_f32_16x16x32_bf16 v[18:21], v[182:185], v[198:201], v[18:21]
	v_mfma_f32_16x16x32_bf16 v[14:17], v[174:177], v[206:209], v[14:17]
	v_mfma_f32_16x16x32_bf16 v[10:13], v[182:185], v[206:209], v[10:13]
	v_mfma_f32_16x16x32_bf16 v[6:9], v[174:177], v[214:217], v[6:9]
	v_mfma_f32_16x16x32_bf16 v[2:5], v[182:185], v[214:217], v[2:5]
	s_barrier
	s_add_i32 s48, 0, 0x18000
	v_add_u32_e32 v142, s48, v1
	s_add_i32 vcc_lo, 0, 0x1c000
	ds_read_b128 v[154:157], v142
	ds_read_b128 v[158:161], v142 offset:1024
	ds_read_b128 v[162:165], v142 offset:2048
	ds_read_b128 v[166:169], v142 offset:3072
	v_add_u32_e32 v142, vcc_lo, v1
	ds_read_b128 v[170:173], v142
	ds_read_b128 v[174:177], v142 offset:1024
	ds_read_b128 v[178:181], v142 offset:2048
	ds_read_b128 v[182:185], v142 offset:3072
	s_mov_b32 m0, s41
	v_lshl_add_u64 v[226:227], s[34:35], 0, v[138:139]
	ds_read_b128 v[186:189], v152 offset:32768
	ds_read_b128 v[190:193], v152 offset:33792
	ds_read_b128 v[194:197], v152 offset:34816
	ds_read_b128 v[198:201], v152 offset:35840
	ds_read_b128 v[202:205], v152 offset:36864
	ds_read_b128 v[206:209], v152 offset:37888
	ds_read_b128 v[210:213], v152 offset:38912
	ds_read_b128 v[214:217], v152 offset:39936
	global_load_lds_dwordx4 v[226:227], off
	v_lshl_add_u64 v[226:227], s[34:35], 0, v[140:141]
	s_mov_b32 m0, s42
	s_nop 0
	global_load_lds_dwordx4 v[226:227], off
	s_waitcnt vmcnt(8)
	s_waitcnt lgkmcnt(0)
	s_barrier
	s_waitcnt lgkmcnt(0)
	v_mfma_f32_16x16x32_bf16 v[126:129], v[154:157], v[186:189], v[126:129]
	v_mfma_f32_16x16x32_bf16 v[122:125], v[162:165], v[186:189], v[122:125]
	v_mfma_f32_16x16x32_bf16 v[118:121], v[154:157], v[194:197], v[118:121]
	v_mfma_f32_16x16x32_bf16 v[114:117], v[162:165], v[194:197], v[114:117]
	v_mfma_f32_16x16x32_bf16 v[110:113], v[154:157], v[202:205], v[110:113]
	v_mfma_f32_16x16x32_bf16 v[106:109], v[162:165], v[202:205], v[106:109]
	v_mfma_f32_16x16x32_bf16 v[102:105], v[154:157], v[210:213], v[102:105]
	v_mfma_f32_16x16x32_bf16 v[98:101], v[162:165], v[210:213], v[98:101]
	v_mfma_f32_16x16x32_bf16 v[126:129], v[158:161], v[190:193], v[126:129]
	v_mfma_f32_16x16x32_bf16 v[122:125], v[166:169], v[190:193], v[122:125]
	v_mfma_f32_16x16x32_bf16 v[118:121], v[158:161], v[198:201], v[118:121]
	v_mfma_f32_16x16x32_bf16 v[114:117], v[166:169], v[198:201], v[114:117]
	v_mfma_f32_16x16x32_bf16 v[110:113], v[158:161], v[206:209], v[110:113]
	v_mfma_f32_16x16x32_bf16 v[106:109], v[166:169], v[206:209], v[106:109]
	v_mfma_f32_16x16x32_bf16 v[102:105], v[158:161], v[214:217], v[102:105]
	v_mfma_f32_16x16x32_bf16 v[98:101], v[166:169], v[214:217], v[98:101]
	v_mfma_f32_16x16x32_bf16 v[94:97], v[170:173], v[186:189], v[94:97]
	v_mfma_f32_16x16x32_bf16 v[90:93], v[178:181], v[186:189], v[90:93]
	v_mfma_f32_16x16x32_bf16 v[86:89], v[170:173], v[194:197], v[86:89]
	v_mfma_f32_16x16x32_bf16 v[82:85], v[178:181], v[194:197], v[82:85]
	v_mfma_f32_16x16x32_bf16 v[78:81], v[170:173], v[202:205], v[78:81]
	v_mfma_f32_16x16x32_bf16 v[74:77], v[178:181], v[202:205], v[74:77]
	v_mfma_f32_16x16x32_bf16 v[70:73], v[170:173], v[210:213], v[70:73]
	v_mfma_f32_16x16x32_bf16 v[66:69], v[178:181], v[210:213], v[66:69]
	v_mfma_f32_16x16x32_bf16 v[94:97], v[174:177], v[190:193], v[94:97]
	v_mfma_f32_16x16x32_bf16 v[90:93], v[182:185], v[190:193], v[90:93]
	v_mfma_f32_16x16x32_bf16 v[86:89], v[174:177], v[198:201], v[86:89]
	v_mfma_f32_16x16x32_bf16 v[82:85], v[182:185], v[198:201], v[82:85]
	v_mfma_f32_16x16x32_bf16 v[78:81], v[174:177], v[206:209], v[78:81]
	v_mfma_f32_16x16x32_bf16 v[74:77], v[182:185], v[206:209], v[74:77]
	v_mfma_f32_16x16x32_bf16 v[70:73], v[174:177], v[214:217], v[70:73]
	v_mfma_f32_16x16x32_bf16 v[66:69], v[182:185], v[214:217], v[66:69]
	s_barrier
; #define PG8_STAGE(bufoff, gbase, v0, v1) do { \
;         __builtin_amdgcn_global_load_lds((const unsigned*)((const char*)(gbase) + (v0)), (LAS unsigned*)(lds + (bufoff) + ldsw), 16, 0, 0); \
;         __builtin_amdgcn_global_load_lds((const unsigned*)((const char*)(gbase) + (v1)), (LAS unsigned*)(lds + (bufoff) + ldsw + 8192), 16, 0, 0); } while (0)
; #define PG8_LDA(dst, b, h) do { _Pragma("unroll") for (int m = 0; m < 4; ++m) { const v4i lo_ = *(const LAS v4i*)(lds + PG8_SA(b, h) + aoff + m * 2048), hi_ = *(const LAS v4i*)(lds + PG8_SA(b, h) + aoff + m * 2048 + 1024); \
;         dst[m] = __builtin_shufflevector(lo_, hi_, 0, 1, 2, 3, 4, 5, 6, 7); } } while (0)
; #define PG8_WAIT_V(n) asm volatile("s_waitcnt vmcnt(" #n ")" ::: "memory")
; #define PG8_WAIT_L(n) asm volatile("s_waitcnt lgkmcnt(" #n ")" ::: "memory")
; #define PG8_BAR __builtin_amdgcn_s_barrier()
; #define PG8_SCHED __builtin_amdgcn_sched_barrier(0)
; template <class Epi, class Sched, bool FP8 = false>
; __device__ __forceinline__ void gemm_phase(LAS unsigned char* lds, const int K, const Sched& S, const Epi& E) {
;     ...
;             PG8_LDA(At, 1, 1); PG8_STAGE(PG8_SB(1, 0), b3, voffB[0], voffB[1]); PG8_STAGE(PG8_SB(1, 1), b3 + hstepB, voffB[0], voffB[1]); PG8_STAGE(PG8_SA(1, 0), a3, x0, x1);
;             PG8_WAIT_V(8); PG8_WAIT_L(0); PG8_BAR; if (!lo_only) { PG8_MMA(1, 0, At, B0); PG8_MMA(1, 1, At, B1); } PG8_BAR; PG8_SCHED;
;         }
;         if (wr == 0) PG8_BAR;
	s_add_i32 s34, s48, s13
	v_lshl_add_u64 v[218:219], v[218:219], 0, s[18:19]
	s_mov_b32 m0, s34
	ds_read_b128 v[186:189], v152 offset:49152
	ds_read_b128 v[190:193], v152 offset:50176
	ds_read_b128 v[194:197], v152 offset:51200
	ds_read_b128 v[198:201], v152 offset:52224
	ds_read_b128 v[202:205], v152 offset:53248
	ds_read_b128 v[206:209], v152 offset:54272
	ds_read_b128 v[210:213], v152 offset:55296
	ds_read_b128 v[214:217], v152 offset:56320
	global_load_lds_dwordx4 v[218:219], off
	s_add_i32 m0, s34, 0x2000
	s_add_u32 s34, s80, 0x80080
	v_lshl_add_u64 v[218:219], v[220:221], 0, s[18:19]
	s_addc_u32 s35, s81, 0
	s_add_i32 s48, vcc_lo, s13
	global_load_lds_dwordx4 v[218:219], off
	v_lshl_add_u64 v[218:219], s[34:35], 0, v[130:131]
	s_mov_b32 m0, s48
	s_nop 0
	global_load_lds_dwordx4 v[218:219], off
	v_lshl_add_u64 v[218:219], s[34:35], 0, v[132:133]
	s_add_i32 m0, s48, 0x2000
	s_nop 0
	global_load_lds_dwordx4 v[218:219], off
	v_lshl_add_u64 v[218:219], v[222:223], 0, s[18:19]
	s_mov_b32 m0, s43
	s_nop 0
	global_load_lds_dwordx4 v[218:219], off
	v_lshl_add_u64 v[218:219], v[224:225], 0, s[18:19]
	s_mov_b32 m0, s44
	s_nop 0
	global_load_lds_dwordx4 v[218:219], off
	s_waitcnt vmcnt(8)
	s_waitcnt lgkmcnt(0)
	s_barrier
	s_waitcnt lgkmcnt(0)
	v_mfma_f32_16x16x32_bf16 v[62:65], v[154:157], v[186:189], v[62:65]
	v_mfma_f32_16x16x32_bf16 v[58:61], v[162:165], v[186:189], v[58:61]
	v_mfma_f32_16x16x32_bf16 v[54:57], v[154:157], v[194:197], v[54:57]
	v_mfma_f32_16x16x32_bf16 v[50:53], v[162:165], v[194:197], v[50:53]
	v_mfma_f32_16x16x32_bf16 v[46:49], v[154:157], v[202:205], v[46:49]
	v_mfma_f32_16x16x32_bf16 v[42:45], v[162:165], v[202:205], v[42:45]
	v_mfma_f32_16x16x32_bf16 v[38:41], v[154:157], v[210:213], v[38:41]
	v_mfma_f32_16x16x32_bf16 v[34:37], v[162:165], v[210:213], v[34:37]
	v_mfma_f32_16x16x32_bf16 v[62:65], v[158:161], v[190:193], v[62:65]
	v_mfma_f32_16x16x32_bf16 v[58:61], v[166:169], v[190:193], v[58:61]
	v_mfma_f32_16x16x32_bf16 v[54:57], v[158:161], v[198:201], v[54:57]
	v_mfma_f32_16x16x32_bf16 v[50:53], v[166:169], v[198:201], v[50:53]
	v_mfma_f32_16x16x32_bf16 v[46:49], v[158:161], v[206:209], v[46:49]
	v_mfma_f32_16x16x32_bf16 v[42:45], v[166:169], v[206:209], v[42:45]
	v_mfma_f32_16x16x32_bf16 v[38:41], v[158:161], v[214:217], v[38:41]
	v_mfma_f32_16x16x32_bf16 v[34:37], v[166:169], v[214:217], v[34:37]
	v_mfma_f32_16x16x32_bf16 v[30:33], v[170:173], v[186:189], v[30:33]
	v_mfma_f32_16x16x32_bf16 v[26:29], v[178:181], v[186:189], v[26:29]
	v_mfma_f32_16x16x32_bf16 v[22:25], v[170:173], v[194:197], v[22:25]
	v_mfma_f32_16x16x32_bf16 v[18:21], v[178:181], v[194:197], v[18:21]
	v_mfma_f32_16x16x32_bf16 v[14:17], v[170:173], v[202:205], v[14:17]
	v_mfma_f32_16x16x32_bf16 v[10:13], v[178:181], v[202:205], v[10:13]
	v_mfma_f32_16x16x32_bf16 v[6:9], v[170:173], v[210:213], v[6:9]
	v_mfma_f32_16x16x32_bf16 v[2:5], v[178:181], v[210:213], v[2:5]
	v_mfma_f32_16x16x32_bf16 v[30:33], v[174:177], v[190:193], v[30:33]
	v_mfma_f32_16x16x32_bf16 v[26:29], v[182:185], v[190:193], v[26:29]
	v_mfma_f32_16x16x32_bf16 v[22:25], v[174:177], v[198:201], v[22:25]
	v_mfma_f32_16x16x32_bf16 v[18:21], v[182:185], v[198:201], v[18:21]
	v_mfma_f32_16x16x32_bf16 v[14:17], v[174:177], v[206:209], v[14:17]
	v_mfma_f32_16x16x32_bf16 v[10:13], v[182:185], v[206:209], v[10:13]
	v_mfma_f32_16x16x32_bf16 v[6:9], v[174:177], v[214:217], v[6:9]
	v_mfma_f32_16x16x32_bf16 v[2:5], v[182:185], v[214:217], v[2:5]
	s_barrier
	s_add_i32 s97, s97, 2
	s_add_u32 s70, s70, 0x100
	s_addc_u32 s71, s71, 0
	s_cmp_gt_u32 s97, 29
	s_cbranch_scc0 .LBB0_209
	s_and_b64 vcc, exec, s[20:21]
	s_cbranch_vccz .LBB0_212
	s_barrier

; __device__ __forceinline__ unsigned xb_ld(unsigned* p)              { return __hip_atomic_load(p, __ATOMIC_RELAXED, __HIP_MEMORY_SCOPE_AGENT); }
; #define RUNPH(k, ...) do { if (IN(k)) { { PH_IDS __VA_ARGS__ } if (REP_PHASE == (k)) { xcd_barrier(bar); { PH_IDS __VA_ARGS__ } } SEAM(k); } } while (0)
; __global__ void __launch_bounds__(512, 2) fwd(Args args) {
;     ...
;         if (IN(3)) { if (G == 256) {
;                 asm volatile("s_waitcnt vmcnt(0)" ::: "memory"); __syncthreads();
;                 if (threadIdx.x == 0) { unsigned* dn = (unsigned*)(ws + WS_CTL) + CTL_INPROJ_DONE; unsigned sp = 0;
;                     while (xb_ld(dn) < 256u) { __builtin_amdgcn_s_sleep(1); if (++sp > XB_SPIN_CAP) break; }
;                     __builtin_amdgcn_fence(__ATOMIC_ACQUIRE, "agent"); }
;                 __syncthreads(); }
;             else xcd_barrier(bar); } }
;     ...
;     RUNPH(3, for (int r_ = 0; r_ < P3_REP_PREP; ++r_) phase3_prep(args, lds, tid, vcu, G, bx); for (int r_ = 0; r_ < P3_REP_POOL; ++r_) phase3_pool(args, lds, tid, vcu, G););
.LBB0_316:
	s_setprio 0
	s_cmp_gt_i32 s94, 3
	s_cselect_b64 s[0:1], -1, 0
	s_cmp_lt_i32 s95, 4
	s_cselect_b64 s[2:3], -1, 0
	s_or_b64 s[0:1], s[0:1], s[2:3]
	s_and_b64 vcc, exec, s[0:1]
	s_cbranch_vccnz .LBB0_764
	v_mov_b32_e32 v66, v0
	s_mov_b32 s99, 0
	s_branch .LBB0_673

; #define PG8_STAGE(bufoff, gbase, v0, v1) do { \
;         __builtin_amdgcn_global_load_lds((const unsigned*)((const char*)(gbase) + (v0)), (LAS unsigned*)(lds + (bufoff) + ldsw), 16, 0, 0); \
;         __builtin_amdgcn_global_load_lds((const unsigned*)((const char*)(gbase) + (v1)), (LAS unsigned*)(lds + (bufoff) + ldsw + 8192), 16, 0, 0); } while (0)
; #define PG8_LDA(dst, b, h) do { _Pragma("unroll") for (int m = 0; m < 4; ++m) { const v4i lo_ = *(const LAS v4i*)(lds + PG8_SA(b, h) + aoff + m * 2048), hi_ = *(const LAS v4i*)(lds + PG8_SA(b, h) + aoff + m * 2048 + 1024); \
;         dst[m] = __builtin_shufflevector(lo_, hi_, 0, 1, 2, 3, 4, 5, 6, 7); } } while (0)
; #define PG8_LDB(dst, b, h) do { _Pragma("unroll") for (int n = 0; n < 2; ++n) { const v4i lo_ = *(const LAS v4i*)(lds + PG8_SB(b, h) + boff + n * 2048), hi_ = *(const LAS v4i*)(lds + PG8_SB(b, h) + boff + n * 2048 + 1024); \
;         dst[n] = __builtin_shufflevector(lo_, hi_, 0, 1, 2, 3, 4, 5, 6, 7); } } while (0)
; #define PG8_WAIT_V(n) asm volatile("s_waitcnt vmcnt(" #n ")" ::: "memory")
; #define PG8_WAIT_L(n) asm volatile("s_waitcnt lgkmcnt(" #n ")" ::: "memory")
; #define PG8_BAR __builtin_amdgcn_s_barrier()
; #define PG8_SCHED __builtin_amdgcn_sched_barrier(0)
; template <class Epi, class Sched, bool FP8 = false>
; __device__ __forceinline__ void gemm_phase(LAS unsigned char* lds, const int K, const Sched& S, const Epi& E) {
;     ...
;             PG8_LDB(B0, 0, 0); PG8_LDB(B1, 0, 1); PG8_SCHED; PG8_LDA(At, 0, 0); PG8_STAGE(PG8_SA(1, 1), a1, vA[2], vA[3]);
;             PG8_WAIT_V(8); PG8_WAIT_L(0); PG8_BAR; PG8_MMA(0, 0, At, B0); PG8_MMA(0, 1, At, B1); PG8_BAR; PG8_SCHED;
;             PG8_LDA(At, 0, 1); PG8_STAGE(PG8_SB(0, 0), b2, voffB[0], voffB[1]); PG8_STAGE(PG8_SB(0, 1), b2 + hstepB, voffB[0], voffB[1]); PG8_STAGE(PG8_SA(0, 0), a2, x0, x1);
;             PG8_WAIT_V(8); PG8_WAIT_L(0); PG8_BAR; if (!lo_only) { PG8_MMA(1, 0, At, B0); PG8_MMA(1, 1, At, B1); } PG8_BAR; PG8_SCHED;
.LBB0_946:
	ds_read_b128 v[146:149], v152
	ds_read_b128 v[156:159], v152 offset:1024
	ds_read_b128 v[160:163], v152 offset:2048
	ds_read_b128 v[164:167], v152 offset:3072
	ds_read_b128 v[168:171], v153
	ds_read_b128 v[172:175], v153 offset:1024
	ds_read_b128 v[176:179], v153 offset:2048
	ds_read_b128 v[180:183], v153 offset:3072
	s_add_i32 s71, s2, 2
	s_add_u32 s42, s34, 0x100
	s_addc_u32 s43, s35, 0
	s_cmp_eq_u32 s48, s2
	s_cselect_b32 s2, s24, s42
	s_cselect_b32 s3, s25, s43
	s_cselect_b32 s73, s27, s70
	s_cselect_b32 s72, s26, s23
	v_lshl_add_u64 v[150:151], s[34:35], 0, v[142:143]
	s_add_i32 m0, s31, 0xc000
	ds_read_b128 v[184:187], v154
	ds_read_b128 v[188:191], v154 offset:1024
	ds_read_b128 v[192:195], v154 offset:2048
	ds_read_b128 v[196:199], v154 offset:3072
	ds_read_b128 v[200:203], v154 offset:4096
	ds_read_b128 v[204:207], v154 offset:5120
	ds_read_b128 v[208:211], v154 offset:6144
	ds_read_b128 v[212:215], v154 offset:7168
	global_load_lds_dwordx4 v[150:151], off
	v_lshl_add_u64 v[150:151], s[34:35], 0, v[144:145]
	s_add_i32 m0, s31, 0xe000
	s_nop 0
	global_load_lds_dwordx4 v[150:151], off
	s_waitcnt vmcnt(8)
	s_waitcnt lgkmcnt(0)
	s_barrier
	s_waitcnt lgkmcnt(0)
	v_mfma_f32_16x16x32_bf16 v[126:129], v[146:149], v[184:187], v[126:129]
	v_mfma_f32_16x16x32_bf16 v[122:125], v[160:163], v[184:187], v[122:125]
	v_mfma_f32_16x16x32_bf16 v[110:113], v[146:149], v[192:195], v[110:113]
	v_mfma_f32_16x16x32_bf16 v[106:109], v[160:163], v[192:195], v[106:109]
	v_mfma_f32_16x16x32_bf16 v[94:97], v[146:149], v[200:203], v[94:97]
	v_mfma_f32_16x16x32_bf16 v[90:93], v[160:163], v[200:203], v[90:93]
	v_mfma_f32_16x16x32_bf16 v[78:81], v[146:149], v[208:211], v[78:81]
	v_mfma_f32_16x16x32_bf16 v[74:77], v[160:163], v[208:211], v[74:77]
	v_mfma_f32_16x16x32_bf16 v[126:129], v[156:159], v[188:191], v[126:129]
	v_mfma_f32_16x16x32_bf16 v[122:125], v[164:167], v[188:191], v[122:125]
	v_mfma_f32_16x16x32_bf16 v[110:113], v[156:159], v[196:199], v[110:113]
	v_mfma_f32_16x16x32_bf16 v[106:109], v[164:167], v[196:199], v[106:109]
	v_mfma_f32_16x16x32_bf16 v[94:97], v[156:159], v[204:207], v[94:97]
	v_mfma_f32_16x16x32_bf16 v[90:93], v[164:167], v[204:207], v[90:93]
	v_mfma_f32_16x16x32_bf16 v[78:81], v[156:159], v[212:215], v[78:81]
	v_mfma_f32_16x16x32_bf16 v[74:77], v[164:167], v[212:215], v[74:77]
	v_mfma_f32_16x16x32_bf16 v[118:121], v[168:171], v[184:187], v[118:121]
	v_mfma_f32_16x16x32_bf16 v[114:117], v[176:179], v[184:187], v[114:117]
	v_mfma_f32_16x16x32_bf16 v[102:105], v[168:171], v[192:195], v[102:105]
	v_mfma_f32_16x16x32_bf16 v[98:101], v[176:179], v[192:195], v[98:101]
	v_mfma_f32_16x16x32_bf16 v[86:89], v[168:171], v[200:203], v[86:89]
	v_mfma_f32_16x16x32_bf16 v[82:85], v[176:179], v[200:203], v[82:85]
	v_mfma_f32_16x16x32_bf16 v[70:73], v[168:171], v[208:211], v[70:73]
	v_mfma_f32_16x16x32_bf16 v[66:69], v[176:179], v[208:211], v[66:69]
	v_mfma_f32_16x16x32_bf16 v[118:121], v[172:175], v[188:191], v[118:121]
	v_mfma_f32_16x16x32_bf16 v[114:117], v[180:183], v[188:191], v[114:117]
	v_mfma_f32_16x16x32_bf16 v[102:105], v[172:175], v[196:199], v[102:105]
	v_mfma_f32_16x16x32_bf16 v[98:101], v[180:183], v[196:199], v[98:101]
	v_mfma_f32_16x16x32_bf16 v[86:89], v[172:175], v[204:207], v[86:89]
	v_mfma_f32_16x16x32_bf16 v[82:85], v[180:183], v[204:207], v[82:85]
	v_mfma_f32_16x16x32_bf16 v[70:73], v[172:175], v[212:215], v[70:73]
	v_mfma_f32_16x16x32_bf16 v[66:69], v[180:183], v[212:215], v[66:69]
	s_barrier
	s_add_i32 s34, s49, s38
	v_lshl_add_u64 v[150:151], s[72:73], 0, v[132:133]
	s_mov_b32 m0, s34
	ds_read_b128 v[184:187], v154 offset:16384
	ds_read_b128 v[188:191], v154 offset:17408
	ds_read_b128 v[192:195], v154 offset:18432
	ds_read_b128 v[196:199], v154 offset:19456
	ds_read_b128 v[200:203], v154 offset:20480
	ds_read_b128 v[204:207], v154 offset:21504
	ds_read_b128 v[208:211], v154 offset:22528
	ds_read_b128 v[212:215], v154 offset:23552
	global_load_lds_dwordx4 v[150:151], off
	s_add_i32 m0, s34, 0x2000
	s_add_u32 s34, s72, s4
	v_lshl_add_u64 v[216:217], s[72:73], 0, v[130:131]
	s_addc_u32 s35, s73, s5
	s_add_i32 s72, s50, s38
	global_load_lds_dwordx4 v[216:217], off
	v_lshl_add_u64 v[218:219], s[34:35], 0, v[132:133]
	s_mov_b32 m0, s72
	v_lshl_add_u64 v[220:221], s[34:35], 0, v[130:131]
	global_load_lds_dwordx4 v[218:219], off
	s_add_i32 m0, s72, 0x2000
	v_lshl_add_u64 v[222:223], s[2:3], 0, v[134:135]
	global_load_lds_dwordx4 v[220:221], off
	s_mov_b32 m0, s31
	v_lshl_add_u64 v[224:225], s[2:3], 0, v[136:137]
	global_load_lds_dwordx4 v[222:223], off
	s_mov_b32 m0, s39
	s_nop 0
	global_load_lds_dwordx4 v[224:225], off
	s_waitcnt vmcnt(8)
	s_waitcnt lgkmcnt(0)
	s_barrier
; #define PG8_STAGE(bufoff, gbase, v0, v1) do { \
;         __builtin_amdgcn_global_load_lds((const unsigned*)((const char*)(gbase) + (v0)), (LAS unsigned*)(lds + (bufoff) + ldsw), 16, 0, 0); \
;         __builtin_amdgcn_global_load_lds((const unsigned*)((const char*)(gbase) + (v1)), (LAS unsigned*)(lds + (bufoff) + ldsw + 8192), 16, 0, 0); } while (0)
; #define PG8_LDA(dst, b, h) do { _Pragma("unroll") for (int m = 0; m < 4; ++m) { const v4i lo_ = *(const LAS v4i*)(lds + PG8_SA(b, h) + aoff + m * 2048), hi_ = *(const LAS v4i*)(lds + PG8_SA(b, h) + aoff + m * 2048 + 1024); \
;         dst[m] = __builtin_shufflevector(lo_, hi_, 0, 1, 2, 3, 4, 5, 6, 7); } } while (0)
; #define PG8_LDB(dst, b, h) do { _Pragma("unroll") for (int n = 0; n < 2; ++n) { const v4i lo_ = *(const LAS v4i*)(lds + PG8_SB(b, h) + boff + n * 2048), hi_ = *(const LAS v4i*)(lds + PG8_SB(b, h) + boff + n * 2048 + 1024); \
;         dst[n] = __builtin_shufflevector(lo_, hi_, 0, 1, 2, 3, 4, 5, 6, 7); } } while (0)
; #define PG8_WAIT_V(n) asm volatile("s_waitcnt vmcnt(" #n ")" ::: "memory")
; #define PG8_WAIT_L(n) asm volatile("s_waitcnt lgkmcnt(" #n ")" ::: "memory")
; #define PG8_BAR __builtin_amdgcn_s_barrier()
; #define PG8_SCHED __builtin_amdgcn_sched_barrier(0)
; template <class Epi, class Sched, bool FP8 = false>
; __device__ __forceinline__ void gemm_phase(LAS unsigned char* lds, const int K, const Sched& S, const Epi& E) {
;     ...
;             PG8_WAIT_V(8); PG8_WAIT_L(0); PG8_BAR; if (!lo_only) { PG8_MMA(1, 0, At, B0); PG8_MMA(1, 1, At, B1); } PG8_BAR; PG8_SCHED;
;             PG8_LDB(B0, 1, 0); PG8_LDB(B1, 1, 1); PG8_SCHED; PG8_LDA(At, 1, 0); PG8_STAGE(PG8_SA(0, 1), a2, x2, x3);
;             PG8_WAIT_V(8); PG8_WAIT_L(0); PG8_BAR; PG8_MMA(0, 0, At, B0); PG8_MMA(0, 1, At, B1); PG8_BAR; PG8_SCHED;
;             PG8_LDA(At, 1, 1); PG8_STAGE(PG8_SB(1, 0), b3, voffB[0], voffB[1]); PG8_STAGE(PG8_SB(1, 1), b3 + hstepB, voffB[0], voffB[1]); PG8_STAGE(PG8_SA(1, 0), a3, x0, x1);
	s_waitcnt lgkmcnt(0)
	v_mfma_f32_16x16x32_bf16 v[62:65], v[146:149], v[184:187], v[62:65]
	v_mfma_f32_16x16x32_bf16 v[58:61], v[160:163], v[184:187], v[58:61]
	v_mfma_f32_16x16x32_bf16 v[46:49], v[146:149], v[192:195], v[46:49]
	v_mfma_f32_16x16x32_bf16 v[42:45], v[160:163], v[192:195], v[42:45]
	v_mfma_f32_16x16x32_bf16 v[30:33], v[146:149], v[200:203], v[30:33]
	v_mfma_f32_16x16x32_bf16 v[26:29], v[160:163], v[200:203], v[26:29]
	v_mfma_f32_16x16x32_bf16 v[14:17], v[146:149], v[208:211], v[14:17]
	v_mfma_f32_16x16x32_bf16 v[10:13], v[160:163], v[208:211], v[10:13]
	v_mfma_f32_16x16x32_bf16 v[62:65], v[156:159], v[188:191], v[62:65]
	v_mfma_f32_16x16x32_bf16 v[58:61], v[164:167], v[188:191], v[58:61]
	v_mfma_f32_16x16x32_bf16 v[46:49], v[156:159], v[196:199], v[46:49]
	v_mfma_f32_16x16x32_bf16 v[42:45], v[164:167], v[196:199], v[42:45]
	v_mfma_f32_16x16x32_bf16 v[30:33], v[156:159], v[204:207], v[30:33]
	v_mfma_f32_16x16x32_bf16 v[26:29], v[164:167], v[204:207], v[26:29]
	v_mfma_f32_16x16x32_bf16 v[14:17], v[156:159], v[212:215], v[14:17]
	v_mfma_f32_16x16x32_bf16 v[10:13], v[164:167], v[212:215], v[10:13]
	v_mfma_f32_16x16x32_bf16 v[54:57], v[168:171], v[184:187], v[54:57]
	v_mfma_f32_16x16x32_bf16 v[50:53], v[176:179], v[184:187], v[50:53]
	v_mfma_f32_16x16x32_bf16 v[38:41], v[168:171], v[192:195], v[38:41]
	v_mfma_f32_16x16x32_bf16 v[34:37], v[176:179], v[192:195], v[34:37]
	v_mfma_f32_16x16x32_bf16 v[22:25], v[168:171], v[200:203], v[22:25]
	v_mfma_f32_16x16x32_bf16 v[18:21], v[176:179], v[200:203], v[18:21]
	v_mfma_f32_16x16x32_bf16 v[6:9], v[168:171], v[208:211], v[6:9]
	v_mfma_f32_16x16x32_bf16 v[2:5], v[176:179], v[208:211], v[2:5]
	v_mfma_f32_16x16x32_bf16 v[54:57], v[172:175], v[188:191], v[54:57]
	v_mfma_f32_16x16x32_bf16 v[50:53], v[180:183], v[188:191], v[50:53]
	v_mfma_f32_16x16x32_bf16 v[38:41], v[172:175], v[196:199], v[38:41]
	v_mfma_f32_16x16x32_bf16 v[34:37], v[180:183], v[196:199], v[34:37]
	v_mfma_f32_16x16x32_bf16 v[22:25], v[172:175], v[204:207], v[22:25]
	v_mfma_f32_16x16x32_bf16 v[18:21], v[180:183], v[204:207], v[18:21]
	v_mfma_f32_16x16x32_bf16 v[6:9], v[172:175], v[212:215], v[6:9]
	v_mfma_f32_16x16x32_bf16 v[2:5], v[180:183], v[212:215], v[2:5]
	s_barrier
	s_add_i32 s34, 0, 0x18000
	s_add_i32 s35, 0, 0x1c000
	v_add_u32_e32 v164, s34, v1
	v_add_u32_e32 v180, s35, v1
	ds_read_b128 v[146:149], v164
	ds_read_b128 v[156:159], v164 offset:1024
	ds_read_b128 v[160:163], v164 offset:2048
	ds_read_b128 v[164:167], v164 offset:3072
	ds_read_b128 v[168:171], v180
	ds_read_b128 v[172:175], v180 offset:1024
	ds_read_b128 v[176:179], v180 offset:2048
	ds_read_b128 v[180:183], v180 offset:3072
	s_mov_b32 m0, s40
	v_lshl_add_u64 v[226:227], s[2:3], 0, v[138:139]
	ds_read_b128 v[184:187], v154 offset:32768
	ds_read_b128 v[188:191], v154 offset:33792
	ds_read_b128 v[192:195], v154 offset:34816
	ds_read_b128 v[196:199], v154 offset:35840
	ds_read_b128 v[200:203], v154 offset:36864
	ds_read_b128 v[204:207], v154 offset:37888
	ds_read_b128 v[208:211], v154 offset:38912
	ds_read_b128 v[212:215], v154 offset:39936
	global_load_lds_dwordx4 v[226:227], off
	v_lshl_add_u64 v[226:227], s[2:3], 0, v[140:141]
	s_mov_b32 m0, s41
	s_nop 0
	global_load_lds_dwordx4 v[226:227], off
	s_waitcnt vmcnt(8)
	s_waitcnt lgkmcnt(0)
	s_barrier
	s_waitcnt lgkmcnt(0)
	v_mfma_f32_16x16x32_bf16 v[126:129], v[146:149], v[184:187], v[126:129]
	v_mfma_f32_16x16x32_bf16 v[122:125], v[160:163], v[184:187], v[122:125]
	v_mfma_f32_16x16x32_bf16 v[110:113], v[146:149], v[192:195], v[110:113]
	v_mfma_f32_16x16x32_bf16 v[106:109], v[160:163], v[192:195], v[106:109]
	v_mfma_f32_16x16x32_bf16 v[94:97], v[146:149], v[200:203], v[94:97]
	v_mfma_f32_16x16x32_bf16 v[90:93], v[160:163], v[200:203], v[90:93]
	v_mfma_f32_16x16x32_bf16 v[78:81], v[146:149], v[208:211], v[78:81]
	v_mfma_f32_16x16x32_bf16 v[74:77], v[160:163], v[208:211], v[74:77]
	v_mfma_f32_16x16x32_bf16 v[126:129], v[156:159], v[188:191], v[126:129]
	v_mfma_f32_16x16x32_bf16 v[122:125], v[164:167], v[188:191], v[122:125]
	v_mfma_f32_16x16x32_bf16 v[110:113], v[156:159], v[196:199], v[110:113]
	v_mfma_f32_16x16x32_bf16 v[106:109], v[164:167], v[196:199], v[106:109]
	v_mfma_f32_16x16x32_bf16 v[94:97], v[156:159], v[204:207], v[94:97]
	v_mfma_f32_16x16x32_bf16 v[90:93], v[164:167], v[204:207], v[90:93]
	v_mfma_f32_16x16x32_bf16 v[78:81], v[156:159], v[212:215], v[78:81]
	v_mfma_f32_16x16x32_bf16 v[74:77], v[164:167], v[212:215], v[74:77]
	v_mfma_f32_16x16x32_bf16 v[118:121], v[168:171], v[184:187], v[118:121]
	v_mfma_f32_16x16x32_bf16 v[114:117], v[176:179], v[184:187], v[114:117]
	v_mfma_f32_16x16x32_bf16 v[102:105], v[168:171], v[192:195], v[102:105]
	v_mfma_f32_16x16x32_bf16 v[98:101], v[176:179], v[192:195], v[98:101]
	v_mfma_f32_16x16x32_bf16 v[86:89], v[168:171], v[200:203], v[86:89]
	v_mfma_f32_16x16x32_bf16 v[82:85], v[176:179], v[200:203], v[82:85]
	v_mfma_f32_16x16x32_bf16 v[70:73], v[168:171], v[208:211], v[70:73]
	v_mfma_f32_16x16x32_bf16 v[66:69], v[176:179], v[208:211], v[66:69]
	v_mfma_f32_16x16x32_bf16 v[118:121], v[172:175], v[188:191], v[118:121]
	v_mfma_f32_16x16x32_bf16 v[114:117], v[180:183], v[188:191], v[114:117]
	v_mfma_f32_16x16x32_bf16 v[102:105], v[172:175], v[196:199], v[102:105]
	v_mfma_f32_16x16x32_bf16 v[98:101], v[180:183], v[196:199], v[98:101]
	v_mfma_f32_16x16x32_bf16 v[86:89], v[172:175], v[204:207], v[86:89]
	v_mfma_f32_16x16x32_bf16 v[82:85], v[180:183], v[204:207], v[82:85]
	v_mfma_f32_16x16x32_bf16 v[70:73], v[172:175], v[212:215], v[70:73]
	v_mfma_f32_16x16x32_bf16 v[66:69], v[180:183], v[212:215], v[66:69]
	s_barrier
; #define PG8_STAGE(bufoff, gbase, v0, v1) do { \
;         __builtin_amdgcn_global_load_lds((const unsigned*)((const char*)(gbase) + (v0)), (LAS unsigned*)(lds + (bufoff) + ldsw), 16, 0, 0); \
;         __builtin_amdgcn_global_load_lds((const unsigned*)((const char*)(gbase) + (v1)), (LAS unsigned*)(lds + (bufoff) + ldsw + 8192), 16, 0, 0); } while (0)
; #define PG8_LDA(dst, b, h) do { _Pragma("unroll") for (int m = 0; m < 4; ++m) { const v4i lo_ = *(const LAS v4i*)(lds + PG8_SA(b, h) + aoff + m * 2048), hi_ = *(const LAS v4i*)(lds + PG8_SA(b, h) + aoff + m * 2048 + 1024); \
;         dst[m] = __builtin_shufflevector(lo_, hi_, 0, 1, 2, 3, 4, 5, 6, 7); } } while (0)
; #define PG8_WAIT_V(n) asm volatile("s_waitcnt vmcnt(" #n ")" ::: "memory")
; #define PG8_WAIT_L(n) asm volatile("s_waitcnt lgkmcnt(" #n ")" ::: "memory")
; #define PG8_BAR __builtin_amdgcn_s_barrier()
; #define PG8_SCHED __builtin_amdgcn_sched_barrier(0)
; template <class Epi, class Sched, bool FP8 = false>
; __device__ __forceinline__ void gemm_phase(LAS unsigned char* lds, const int K, const Sched& S, const Epi& E) {
;     ...
;             PG8_LDA(At, 1, 1); PG8_STAGE(PG8_SB(1, 0), b3, voffB[0], voffB[1]); PG8_STAGE(PG8_SB(1, 1), b3 + hstepB, voffB[0], voffB[1]); PG8_STAGE(PG8_SA(1, 0), a3, x0, x1);
;             PG8_WAIT_V(8); PG8_WAIT_L(0); PG8_BAR; if (!lo_only) { PG8_MMA(1, 0, At, B0); PG8_MMA(1, 1, At, B1); } PG8_BAR; PG8_SCHED;
;         }
;         if (wr == 0) PG8_BAR;
	s_add_i32 s2, s34, s38
	v_lshl_add_u64 v[150:151], v[150:151], 0, s[10:11]
	s_mov_b32 m0, s2
	ds_read_b128 v[184:187], v154 offset:49152
	ds_read_b128 v[188:191], v154 offset:50176
	ds_read_b128 v[192:195], v154 offset:51200
	ds_read_b128 v[196:199], v154 offset:52224
	ds_read_b128 v[200:203], v154 offset:53248
	ds_read_b128 v[204:207], v154 offset:54272
	ds_read_b128 v[208:211], v154 offset:55296
	ds_read_b128 v[212:215], v154 offset:56320
	global_load_lds_dwordx4 v[150:151], off
	v_lshl_add_u64 v[150:151], v[216:217], 0, s[10:11]
	s_add_i32 m0, s2, 0x2000
	s_add_i32 s2, s35, s38
	global_load_lds_dwordx4 v[150:151], off
	v_lshl_add_u64 v[150:151], v[218:219], 0, s[10:11]
	s_mov_b32 m0, s2
	s_nop 0
	global_load_lds_dwordx4 v[150:151], off
	v_lshl_add_u64 v[150:151], v[220:221], 0, s[10:11]
	s_add_i32 m0, s2, 0x2000
	s_nop 0
	global_load_lds_dwordx4 v[150:151], off
	v_lshl_add_u64 v[150:151], v[222:223], 0, s[10:11]
	s_mov_b32 m0, s45
	s_nop 0
	global_load_lds_dwordx4 v[150:151], off
	v_lshl_add_u64 v[150:151], v[224:225], 0, s[10:11]
	s_mov_b32 m0, s46
	s_nop 0
	global_load_lds_dwordx4 v[150:151], off
	s_waitcnt vmcnt(8)
	s_waitcnt lgkmcnt(0)
	s_barrier
	s_waitcnt lgkmcnt(0)
	v_mfma_f32_16x16x32_bf16 v[62:65], v[146:149], v[184:187], v[62:65]
	v_mfma_f32_16x16x32_bf16 v[58:61], v[160:163], v[184:187], v[58:61]
	v_mfma_f32_16x16x32_bf16 v[46:49], v[146:149], v[192:195], v[46:49]
	v_mfma_f32_16x16x32_bf16 v[42:45], v[160:163], v[192:195], v[42:45]
	v_mfma_f32_16x16x32_bf16 v[30:33], v[146:149], v[200:203], v[30:33]
	v_mfma_f32_16x16x32_bf16 v[26:29], v[160:163], v[200:203], v[26:29]
	v_mfma_f32_16x16x32_bf16 v[14:17], v[146:149], v[208:211], v[14:17]
	v_mfma_f32_16x16x32_bf16 v[10:13], v[160:163], v[208:211], v[10:13]
	v_mfma_f32_16x16x32_bf16 v[62:65], v[156:159], v[188:191], v[62:65]
	v_mfma_f32_16x16x32_bf16 v[58:61], v[164:167], v[188:191], v[58:61]
	v_mfma_f32_16x16x32_bf16 v[46:49], v[156:159], v[196:199], v[46:49]
	v_mfma_f32_16x16x32_bf16 v[42:45], v[164:167], v[196:199], v[42:45]
	v_mfma_f32_16x16x32_bf16 v[30:33], v[156:159], v[204:207], v[30:33]
	v_mfma_f32_16x16x32_bf16 v[26:29], v[164:167], v[204:207], v[26:29]
	v_mfma_f32_16x16x32_bf16 v[14:17], v[156:159], v[212:215], v[14:17]
	v_mfma_f32_16x16x32_bf16 v[10:13], v[164:167], v[212:215], v[10:13]
	v_mfma_f32_16x16x32_bf16 v[54:57], v[168:171], v[184:187], v[54:57]
	v_mfma_f32_16x16x32_bf16 v[50:53], v[176:179], v[184:187], v[50:53]
	v_mfma_f32_16x16x32_bf16 v[38:41], v[168:171], v[192:195], v[38:41]
	v_mfma_f32_16x16x32_bf16 v[34:37], v[176:179], v[192:195], v[34:37]
	v_mfma_f32_16x16x32_bf16 v[22:25], v[168:171], v[200:203], v[22:25]
	v_mfma_f32_16x16x32_bf16 v[18:21], v[176:179], v[200:203], v[18:21]
	v_mfma_f32_16x16x32_bf16 v[6:9], v[168:171], v[208:211], v[6:9]
	v_mfma_f32_16x16x32_bf16 v[2:5], v[176:179], v[208:211], v[2:5]
	v_mfma_f32_16x16x32_bf16 v[54:57], v[172:175], v[188:191], v[54:57]
	v_mfma_f32_16x16x32_bf16 v[50:53], v[180:183], v[188:191], v[50:53]
	v_mfma_f32_16x16x32_bf16 v[38:41], v[172:175], v[196:199], v[38:41]
	v_mfma_f32_16x16x32_bf16 v[34:37], v[180:183], v[196:199], v[34:37]
	v_mfma_f32_16x16x32_bf16 v[22:25], v[172:175], v[204:207], v[22:25]
	v_mfma_f32_16x16x32_bf16 v[18:21], v[180:183], v[204:207], v[18:21]
	v_mfma_f32_16x16x32_bf16 v[6:9], v[172:175], v[212:215], v[6:9]
	v_mfma_f32_16x16x32_bf16 v[2:5], v[180:183], v[212:215], v[2:5]
	s_barrier
	s_add_u32 s23, s23, 0x100
	s_addc_u32 s70, s70, 0
	s_cmp_ge_i32 s71, s47
	s_mov_b64 s[34:35], s[42:43]
	s_mov_b32 s2, s71
	s_cbranch_scc0 .LBB0_946

; #define RUNPH(k, ...) do { if (IN(k)) { { PH_IDS __VA_ARGS__ } if (REP_PHASE == (k)) { xcd_barrier(bar); { PH_IDS __VA_ARGS__ } } SEAM(k); } } while (0)
; __global__ void __launch_bounds__(512, 2) fwd(Args args) {
;     ...
;     RUNPH(6, {
;         DenseSched S; S.init(ws + RA_YMIX, ws + WS_WOUT, 1024, 1024, NT, 2048, G, bx);
;         EpiOut E{(bf16*)(ws + RA_Y1)};
;         int kout = 1024; asm volatile("" : "+s"(kout));
;         pg8::gemm_phase<EpiOut, DenseSched, true>(lds, kout, S, E); });
.LBB0_1003:
	s_setprio 0
	v_readfirstlane_b32 s0, v0
	s_nop 3
	s_lshr_b32 s0, s0, 6
	s_cmp_ge_u32 s0, 4
	s_cbranch_scc0 .Lprio_p6
	s_setprio 1

; #define PG8_STAGE(bufoff, gbase, v0, v1) do { \
;         __builtin_amdgcn_global_load_lds((const unsigned*)((const char*)(gbase) + (v0)), (LAS unsigned*)(lds + (bufoff) + ldsw), 16, 0, 0); \
;         __builtin_amdgcn_global_load_lds((const unsigned*)((const char*)(gbase) + (v1)), (LAS unsigned*)(lds + (bufoff) + ldsw + 8192), 16, 0, 0); } while (0)
; #define PG8_LDA(dst, b, h) do { _Pragma("unroll") for (int m = 0; m < 4; ++m) { const v4i lo_ = *(const LAS v4i*)(lds + PG8_SA(b, h) + aoff + m * 2048), hi_ = *(const LAS v4i*)(lds + PG8_SA(b, h) + aoff + m * 2048 + 1024); \
;         dst[m] = __builtin_shufflevector(lo_, hi_, 0, 1, 2, 3, 4, 5, 6, 7); } } while (0)
; #define PG8_LDB(dst, b, h) do { _Pragma("unroll") for (int n = 0; n < 2; ++n) { const v4i lo_ = *(const LAS v4i*)(lds + PG8_SB(b, h) + boff + n * 2048), hi_ = *(const LAS v4i*)(lds + PG8_SB(b, h) + boff + n * 2048 + 1024); \
;         dst[n] = __builtin_shufflevector(lo_, hi_, 0, 1, 2, 3, 4, 5, 6, 7); } } while (0)
; #define PG8_WAIT_V(n) asm volatile("s_waitcnt vmcnt(" #n ")" ::: "memory")
; #define PG8_WAIT_L(n) asm volatile("s_waitcnt lgkmcnt(" #n ")" ::: "memory")
; #define PG8_BAR __builtin_amdgcn_s_barrier()
; #define PG8_SCHED __builtin_amdgcn_sched_barrier(0)
; template <class Epi, class Sched, bool FP8 = false>
; __device__ __forceinline__ void gemm_phase(LAS unsigned char* lds, const int K, const Sched& S, const Epi& E) {
;     ...
;             PG8_LDB(B0, 0, 0); PG8_LDB(B1, 0, 1); PG8_SCHED; PG8_LDA(At, 0, 0); PG8_STAGE(PG8_SA(1, 1), a1, vA[2], vA[3]);
;             PG8_WAIT_V(8); PG8_WAIT_L(0); PG8_BAR; PG8_MMA(0, 0, At, B0); PG8_MMA(0, 1, At, B1); PG8_BAR; PG8_SCHED;
;             PG8_LDA(At, 0, 1); PG8_STAGE(PG8_SB(0, 0), b2, voffB[0], voffB[1]); PG8_STAGE(PG8_SB(0, 1), b2 + hstepB, voffB[0], voffB[1]); PG8_STAGE(PG8_SA(0, 0), a2, x0, x1);
;             PG8_WAIT_V(8); PG8_WAIT_L(0); PG8_BAR; if (!lo_only) { PG8_MMA(1, 0, At, B0); PG8_MMA(1, 1, At, B1); } PG8_BAR; PG8_SCHED;
;             PG8_LDB(B0, 1, 0); PG8_LDB(B1, 1, 1); PG8_SCHED; PG8_LDA(At, 1, 0); PG8_STAGE(PG8_SA(0, 1), a2, x2, x3);
;             PG8_WAIT_V(8); PG8_WAIT_L(0); PG8_BAR; PG8_MMA(0, 0, At, B0); PG8_MMA(0, 1, At, B1); PG8_BAR; PG8_SCHED;
.LBB0_1022:
	ds_read_b128 v[18:21], v194
	ds_read_b128 v[22:25], v194 offset:1024
	ds_read_b128 v[26:29], v194 offset:2048
	ds_read_b128 v[30:33], v194 offset:3072
	ds_read_b128 v[2:5], v195
	ds_read_b128 v[6:9], v195 offset:1024
	ds_read_b128 v[10:13], v195 offset:2048
	ds_read_b128 v[14:17], v195 offset:3072
	s_add_i32 s27, s29, 2
	s_add_u32 s44, s42, 0x100
	s_addc_u32 s45, s43, 0
	s_cmp_eq_u32 s59, s29
	s_cselect_b32 s47, s31, s45
	s_cselect_b32 s46, s30, s44
	s_cselect_b32 s49, s35, s3
	s_cselect_b32 s48, s34, s2
	v_lshl_add_u64 v[190:191], s[42:43], 0, v[174:175]
	s_add_i32 m0, s25, 0xc000
	ds_read_b128 v[182:185], v196
	ds_read_b128 v[186:189], v196 offset:1024
	ds_read_b128 v[198:201], v196 offset:2048
	ds_read_b128 v[202:205], v196 offset:3072
	ds_read_b128 v[206:209], v196 offset:4096
	ds_read_b128 v[210:213], v196 offset:5120
	ds_read_b128 v[214:217], v196 offset:6144
	ds_read_b128 v[218:221], v196 offset:7168
	global_load_lds_dwordx4 v[190:191], off
	v_lshl_add_u64 v[190:191], s[42:43], 0, v[176:177]
	s_add_i32 m0, s25, 0xe000
	s_nop 0
	global_load_lds_dwordx4 v[190:191], off
	s_waitcnt vmcnt(8)
	s_waitcnt lgkmcnt(0)
	s_barrier
	s_nop 4
	s_waitcnt lgkmcnt(0)
	v_mfma_f32_16x16x128_f8f6f4 v[158:161], v[18:25], v[182:189], v[158:161]
	v_mfma_f32_16x16x128_f8f6f4 v[154:157], v[26:33], v[182:189], v[154:157]
	v_mfma_f32_16x16x128_f8f6f4 v[150:153], v[18:25], v[198:205], v[150:153]
	v_mfma_f32_16x16x128_f8f6f4 v[146:149], v[26:33], v[198:205], v[146:149]
	v_mfma_f32_16x16x128_f8f6f4 v[138:141], v[18:25], v[206:213], v[138:141]
	v_mfma_f32_16x16x128_f8f6f4 v[130:133], v[26:33], v[206:213], v[130:133]
	v_mfma_f32_16x16x128_f8f6f4 v[122:125], v[18:25], v[214:221], v[122:125]
	v_mfma_f32_16x16x128_f8f6f4 v[114:117], v[26:33], v[214:221], v[114:117]
	s_nop 4
	v_mfma_f32_16x16x128_f8f6f4 v[142:145], v[2:9], v[182:189], v[142:145]
	v_mfma_f32_16x16x128_f8f6f4 v[134:137], v[10:17], v[182:189], v[134:137]
	v_mfma_f32_16x16x128_f8f6f4 v[126:129], v[2:9], v[198:205], v[126:129]
	v_mfma_f32_16x16x128_f8f6f4 v[118:121], v[10:17], v[198:205], v[118:121]
	v_mfma_f32_16x16x128_f8f6f4 v[110:113], v[2:9], v[206:213], v[110:113]
	v_mfma_f32_16x16x128_f8f6f4 v[106:109], v[10:17], v[206:213], v[106:109]
	v_mfma_f32_16x16x128_f8f6f4 v[102:105], v[2:9], v[214:221], v[102:105]
	v_mfma_f32_16x16x128_f8f6f4 v[98:101], v[10:17], v[214:221], v[98:101]
	s_barrier
	s_add_i32 s29, s71, s39
	v_lshl_add_u64 v[182:183], s[48:49], 0, v[162:163]
	s_mov_b32 m0, s29
	ds_read_b128 v[198:201], v196 offset:16384
	ds_read_b128 v[202:205], v196 offset:17408
	ds_read_b128 v[206:209], v196 offset:18432
	ds_read_b128 v[210:213], v196 offset:19456
	ds_read_b128 v[214:217], v196 offset:20480
	ds_read_b128 v[218:221], v196 offset:21504
	ds_read_b128 v[222:225], v196 offset:22528
	ds_read_b128 v[226:229], v196 offset:23552
	global_load_lds_dwordx4 v[182:183], off
	s_add_i32 m0, s29, 0x2000
	s_add_u32 s42, s48, s4
	v_lshl_add_u64 v[184:185], s[48:49], 0, v[164:165]
	s_addc_u32 s43, s49, s5
	s_add_i32 s29, s72, s39
	global_load_lds_dwordx4 v[184:185], off
	v_lshl_add_u64 v[186:187], s[42:43], 0, v[162:163]
	s_mov_b32 m0, s29
	v_lshl_add_u64 v[188:189], s[42:43], 0, v[164:165]
	global_load_lds_dwordx4 v[186:187], off
	s_add_i32 m0, s29, 0x2000
	v_lshl_add_u64 v[190:191], s[46:47], 0, v[166:167]
	global_load_lds_dwordx4 v[188:189], off
	s_mov_b32 m0, s25
	v_lshl_add_u64 v[192:193], s[46:47], 0, v[168:169]
	global_load_lds_dwordx4 v[190:191], off
	s_mov_b32 m0, s40
	s_nop 0
	global_load_lds_dwordx4 v[192:193], off
	s_waitcnt vmcnt(8)
	s_waitcnt lgkmcnt(0)
	s_barrier
	s_nop 4
	s_waitcnt lgkmcnt(0)
	v_mfma_f32_16x16x128_f8f6f4 v[94:97], v[18:25], v[198:205], v[94:97]
	v_mfma_f32_16x16x128_f8f6f4 v[90:93], v[26:33], v[198:205], v[90:93]
	v_mfma_f32_16x16x128_f8f6f4 v[86:89], v[18:25], v[206:213], v[86:89]
	v_mfma_f32_16x16x128_f8f6f4 v[82:85], v[26:33], v[206:213], v[82:85]
	v_mfma_f32_16x16x128_f8f6f4 v[74:77], v[18:25], v[214:221], v[74:77]
	v_mfma_f32_16x16x128_f8f6f4 v[66:69], v[26:33], v[214:221], v[66:69]
	v_mfma_f32_16x16x128_f8f6f4 v[58:61], v[18:25], v[222:229], v[58:61]
	v_mfma_f32_16x16x128_f8f6f4 v[50:53], v[26:33], v[222:229], v[50:53]
	s_nop 4
	v_mfma_f32_16x16x128_f8f6f4 v[78:81], v[2:9], v[198:205], v[78:81]
	v_mfma_f32_16x16x128_f8f6f4 v[70:73], v[10:17], v[198:205], v[70:73]
	v_mfma_f32_16x16x128_f8f6f4 v[62:65], v[2:9], v[206:213], v[62:65]
	v_mfma_f32_16x16x128_f8f6f4 v[54:57], v[10:17], v[206:213], v[54:57]
	v_mfma_f32_16x16x128_f8f6f4 v[46:49], v[2:9], v[214:221], v[46:49]
	v_mfma_f32_16x16x128_f8f6f4 v[42:45], v[10:17], v[214:221], v[42:45]
	v_mfma_f32_16x16x128_f8f6f4 v[38:41], v[2:9], v[222:229], v[38:41]
	v_mfma_f32_16x16x128_f8f6f4 v[34:37], v[10:17], v[222:229], v[34:37]
	s_barrier
	s_add_i32 s29, 0, 0x18000
	s_add_i32 s42, 0, 0x1c000
	v_add_u32_e32 v14, s29, v1
	v_add_u32_e32 v30, s42, v1
	ds_read_b128 v[2:5], v14
	ds_read_b128 v[6:9], v14 offset:1024
	ds_read_b128 v[10:13], v14 offset:2048
	ds_read_b128 v[14:17], v14 offset:3072
	ds_read_b128 v[18:21], v30
	ds_read_b128 v[22:25], v30 offset:1024
	ds_read_b128 v[26:29], v30 offset:2048
	ds_read_b128 v[30:33], v30 offset:3072
	s_mov_b32 m0, s41
	v_lshl_add_u64 v[230:231], s[46:47], 0, v[170:171]
	ds_read_b128 v[198:201], v196 offset:32768
	ds_read_b128 v[202:205], v196 offset:33792
	ds_read_b128 v[206:209], v196 offset:34816
	ds_read_b128 v[210:213], v196 offset:35840
	ds_read_b128 v[214:217], v196 offset:36864
	ds_read_b128 v[218:221], v196 offset:37888
	ds_read_b128 v[222:225], v196 offset:38912
	ds_read_b128 v[226:229], v196 offset:39936
	global_load_lds_dwordx4 v[230:231], off
	v_lshl_add_u64 v[230:231], s[46:47], 0, v[172:173]
	s_mov_b32 m0, s50
	s_nop 0
	global_load_lds_dwordx4 v[230:231], off
	s_waitcnt vmcnt(8)
	s_waitcnt lgkmcnt(0)
	s_barrier
; #define PG8_STAGE(bufoff, gbase, v0, v1) do { \
;         __builtin_amdgcn_global_load_lds((const unsigned*)((const char*)(gbase) + (v0)), (LAS unsigned*)(lds + (bufoff) + ldsw), 16, 0, 0); \
;         __builtin_amdgcn_global_load_lds((const unsigned*)((const char*)(gbase) + (v1)), (LAS unsigned*)(lds + (bufoff) + ldsw + 8192), 16, 0, 0); } while (0)
; #define PG8_LDA(dst, b, h) do { _Pragma("unroll") for (int m = 0; m < 4; ++m) { const v4i lo_ = *(const LAS v4i*)(lds + PG8_SA(b, h) + aoff + m * 2048), hi_ = *(const LAS v4i*)(lds + PG8_SA(b, h) + aoff + m * 2048 + 1024); \
;         dst[m] = __builtin_shufflevector(lo_, hi_, 0, 1, 2, 3, 4, 5, 6, 7); } } while (0)
; #define PG8_WAIT_V(n) asm volatile("s_waitcnt vmcnt(" #n ")" ::: "memory")
; #define PG8_WAIT_L(n) asm volatile("s_waitcnt lgkmcnt(" #n ")" ::: "memory")
; #define PG8_BAR __builtin_amdgcn_s_barrier()
; #define PG8_SCHED __builtin_amdgcn_sched_barrier(0)
; template <class Epi, class Sched, bool FP8 = false>
; __device__ __forceinline__ void gemm_phase(LAS unsigned char* lds, const int K, const Sched& S, const Epi& E) {
;     ...
;             PG8_WAIT_V(8); PG8_WAIT_L(0); PG8_BAR; PG8_MMA(0, 0, At, B0); PG8_MMA(0, 1, At, B1); PG8_BAR; PG8_SCHED;
;             PG8_LDA(At, 1, 1); PG8_STAGE(PG8_SB(1, 0), b3, voffB[0], voffB[1]); PG8_STAGE(PG8_SB(1, 1), b3 + hstepB, voffB[0], voffB[1]); PG8_STAGE(PG8_SA(1, 0), a3, x0, x1);
;             PG8_WAIT_V(8); PG8_WAIT_L(0); PG8_BAR; if (!lo_only) { PG8_MMA(1, 0, At, B0); PG8_MMA(1, 1, At, B1); } PG8_BAR; PG8_SCHED;
;         }
	s_nop 4
	s_waitcnt lgkmcnt(0)
	v_mfma_f32_16x16x128_f8f6f4 v[158:161], v[2:9], v[198:205], v[158:161]
	v_mfma_f32_16x16x128_f8f6f4 v[154:157], v[10:17], v[198:205], v[154:157]
	v_mfma_f32_16x16x128_f8f6f4 v[150:153], v[2:9], v[206:213], v[150:153]
	v_mfma_f32_16x16x128_f8f6f4 v[146:149], v[10:17], v[206:213], v[146:149]
	v_mfma_f32_16x16x128_f8f6f4 v[138:141], v[2:9], v[214:221], v[138:141]
	v_mfma_f32_16x16x128_f8f6f4 v[130:133], v[10:17], v[214:221], v[130:133]
	v_mfma_f32_16x16x128_f8f6f4 v[122:125], v[2:9], v[222:229], v[122:125]
	v_mfma_f32_16x16x128_f8f6f4 v[114:117], v[10:17], v[222:229], v[114:117]
	s_nop 4
	v_mfma_f32_16x16x128_f8f6f4 v[142:145], v[18:25], v[198:205], v[142:145]
	v_mfma_f32_16x16x128_f8f6f4 v[134:137], v[26:33], v[198:205], v[134:137]
	v_mfma_f32_16x16x128_f8f6f4 v[126:129], v[18:25], v[206:213], v[126:129]
	v_mfma_f32_16x16x128_f8f6f4 v[118:121], v[26:33], v[206:213], v[118:121]
	v_mfma_f32_16x16x128_f8f6f4 v[110:113], v[18:25], v[214:221], v[110:113]
	v_mfma_f32_16x16x128_f8f6f4 v[106:109], v[26:33], v[214:221], v[106:109]
	v_mfma_f32_16x16x128_f8f6f4 v[102:105], v[18:25], v[222:229], v[102:105]
	v_mfma_f32_16x16x128_f8f6f4 v[98:101], v[26:33], v[222:229], v[98:101]
	s_barrier
	s_add_i32 s29, s29, s39
	v_lshl_add_u64 v[182:183], v[182:183], 0, s[10:11]
	s_mov_b32 m0, s29
	ds_read_b128 v[198:201], v196 offset:49152
	ds_read_b128 v[202:205], v196 offset:50176
	ds_read_b128 v[206:209], v196 offset:51200
	ds_read_b128 v[210:213], v196 offset:52224
	ds_read_b128 v[214:217], v196 offset:53248
	ds_read_b128 v[218:221], v196 offset:54272
	ds_read_b128 v[222:225], v196 offset:55296
	ds_read_b128 v[226:229], v196 offset:56320
	global_load_lds_dwordx4 v[182:183], off
	v_lshl_add_u64 v[182:183], v[184:185], 0, s[10:11]
	s_add_i32 m0, s29, 0x2000
	s_add_i32 s29, s42, s39
	global_load_lds_dwordx4 v[182:183], off
	v_lshl_add_u64 v[182:183], v[186:187], 0, s[10:11]
	s_mov_b32 m0, s29
	s_nop 0
	global_load_lds_dwordx4 v[182:183], off
	v_lshl_add_u64 v[182:183], v[188:189], 0, s[10:11]
	s_add_i32 m0, s29, 0x2000
	s_nop 0
	global_load_lds_dwordx4 v[182:183], off
	v_lshl_add_u64 v[182:183], v[190:191], 0, s[10:11]
	s_mov_b32 m0, s54
	s_nop 0
	global_load_lds_dwordx4 v[182:183], off
	v_lshl_add_u64 v[182:183], v[192:193], 0, s[10:11]
	s_mov_b32 m0, s55
	s_nop 0
	global_load_lds_dwordx4 v[182:183], off
	s_waitcnt vmcnt(8)
	s_waitcnt lgkmcnt(0)
	s_barrier
	s_nop 4
	s_waitcnt lgkmcnt(0)
	v_mfma_f32_16x16x128_f8f6f4 v[94:97], v[2:9], v[198:205], v[94:97]
	v_mfma_f32_16x16x128_f8f6f4 v[90:93], v[10:17], v[198:205], v[90:93]
	v_mfma_f32_16x16x128_f8f6f4 v[86:89], v[2:9], v[206:213], v[86:89]
	v_mfma_f32_16x16x128_f8f6f4 v[82:85], v[10:17], v[206:213], v[82:85]
	v_mfma_f32_16x16x128_f8f6f4 v[74:77], v[2:9], v[214:221], v[74:77]
	v_mfma_f32_16x16x128_f8f6f4 v[66:69], v[10:17], v[214:221], v[66:69]
	v_mfma_f32_16x16x128_f8f6f4 v[58:61], v[2:9], v[222:229], v[58:61]
	v_mfma_f32_16x16x128_f8f6f4 v[50:53], v[10:17], v[222:229], v[50:53]
	s_nop 4
	v_mfma_f32_16x16x128_f8f6f4 v[78:81], v[18:25], v[198:205], v[78:81]
	v_mfma_f32_16x16x128_f8f6f4 v[70:73], v[26:33], v[198:205], v[70:73]
	v_mfma_f32_16x16x128_f8f6f4 v[62:65], v[18:25], v[206:213], v[62:65]
	v_mfma_f32_16x16x128_f8f6f4 v[54:57], v[26:33], v[206:213], v[54:57]
	v_mfma_f32_16x16x128_f8f6f4 v[46:49], v[18:25], v[214:221], v[46:49]
	v_mfma_f32_16x16x128_f8f6f4 v[42:45], v[26:33], v[214:221], v[42:45]
	v_mfma_f32_16x16x128_f8f6f4 v[38:41], v[18:25], v[222:229], v[38:41]
	v_mfma_f32_16x16x128_f8f6f4 v[34:37], v[26:33], v[222:229], v[34:37]
	s_barrier
	s_add_u32 s2, s2, 0x100
	s_addc_u32 s3, s3, 0
	s_cmp_ge_i32 s27, s58
	s_mov_b64 s[42:43], s[44:45]
	s_mov_b32 s29, s27
	s_cbranch_scc0 .LBB0_1022
; __device__ __forceinline__ unsigned cvt_pk_bf16(float lo, float hi) { unsigned r; asm volatile("v_cvt_pk_bf16_f32 %0, %1, %2" : "=v"(r) : "v"(lo), "v"(hi)); return r; }
;     __device__ __forceinline__ void operator()(const f32x4 (&acc)[2][2][4][2], const DenseU& u, int wr, int wc, int fr, int fq) const {
;     ...
;             for (int m = 0; m < 4; ++m) { bf16* rp = y + (size_t)(row0 + ai * 128 + m * 16) * 2048 + col0;
; #pragma unroll
;                 for (int bj = 0; bj < 2; ++bj) { constexpr float inv = 1.f / (SC_W * SC_Y); const f32x4 v0 = acc[ai][bj][m][0] * inv, v1 = acc[ai][bj][m][1] * inv;
;                     v4u o; o.x = pg8::cvt_pk_bf16(v0[0], v0[1]); o.y = pg8::cvt_pk_bf16(v0[2], v0[3]); o.z = pg8::cvt_pk_bf16(v1[0], v1[1]); o.w = pg8::cvt_pk_bf16(v1[2], v1[3]);
;                     *(v4u*)(rp + bj * 128) = o; } }
	v_pk_mul_f32 v[2:3], v[160:161], s[16:17] op_sel_hi:[1,0]
	v_pk_mul_f32 v[18:19], v[158:159], s[16:17] op_sel_hi:[1,0]
	v_pk_mul_f32 v[24:25], v[156:157], s[16:17] op_sel_hi:[1,0]
	v_pk_mul_f32 v[32:33], v[154:155], s[16:17] op_sel_hi:[1,0]
	v_pk_mul_f32 v[144:145], v[144:145], s[16:17] op_sel_hi:[1,0]
	v_pk_mul_f32 v[142:143], v[142:143], s[16:17] op_sel_hi:[1,0]
	v_pk_mul_f32 v[136:137], v[136:137], s[16:17] op_sel_hi:[1,0]
	v_pk_mul_f32 v[134:135], v[134:135], s[16:17] op_sel_hi:[1,0]
	v_pk_mul_f32 v[8:9], v[152:153], s[16:17] op_sel_hi:[1,0]
	v_pk_mul_f32 v[14:15], v[150:151], s[16:17] op_sel_hi:[1,0]
	v_pk_mul_f32 v[22:23], v[148:149], s[16:17] op_sel_hi:[1,0]
	v_pk_mul_f32 v[30:31], v[146:147], s[16:17] op_sel_hi:[1,0]
	v_pk_mul_f32 v[128:129], v[128:129], s[16:17] op_sel_hi:[1,0]
	v_pk_mul_f32 v[126:127], v[126:127], s[16:17] op_sel_hi:[1,0]
	v_pk_mul_f32 v[120:121], v[120:121], s[16:17] op_sel_hi:[1,0]
	v_pk_mul_f32 v[118:119], v[118:119], s[16:17] op_sel_hi:[1,0]
	v_pk_mul_f32 v[6:7], v[140:141], s[16:17] op_sel_hi:[1,0]
	v_pk_mul_f32 v[12:13], v[138:139], s[16:17] op_sel_hi:[1,0]
	v_pk_mul_f32 v[20:21], v[132:133], s[16:17] op_sel_hi:[1,0]
	v_pk_mul_f32 v[28:29], v[130:131], s[16:17] op_sel_hi:[1,0]
	v_pk_mul_f32 v[112:113], v[112:113], s[16:17] op_sel_hi:[1,0]
	v_pk_mul_f32 v[110:111], v[110:111], s[16:17] op_sel_hi:[1,0]
	v_pk_mul_f32 v[108:109], v[108:109], s[16:17] op_sel_hi:[1,0]
	v_pk_mul_f32 v[106:107], v[106:107], s[16:17] op_sel_hi:[1,0]
	v_pk_mul_f32 v[4:5], v[124:125], s[16:17] op_sel_hi:[1,0]
	v_pk_mul_f32 v[10:11], v[122:123], s[16:17] op_sel_hi:[1,0]
	v_pk_mul_f32 v[16:17], v[116:117], s[16:17] op_sel_hi:[1,0]
	v_pk_mul_f32 v[26:27], v[114:115], s[16:17] op_sel_hi:[1,0]
	v_pk_mul_f32 v[104:105], v[104:105], s[16:17] op_sel_hi:[1,0]
	v_pk_mul_f32 v[102:103], v[102:103], s[16:17] op_sel_hi:[1,0]
	v_pk_mul_f32 v[100:101], v[100:101], s[16:17] op_sel_hi:[1,0]
	v_pk_mul_f32 v[98:99], v[98:99], s[16:17] op_sel_hi:[1,0]
	v_pk_mul_f32 v[96:97], v[96:97], s[16:17] op_sel_hi:[1,0]
	v_pk_mul_f32 v[94:95], v[94:95], s[16:17] op_sel_hi:[1,0]
	v_pk_mul_f32 v[92:93], v[92:93], s[16:17] op_sel_hi:[1,0]
	v_pk_mul_f32 v[90:91], v[90:91], s[16:17] op_sel_hi:[1,0]
	v_pk_mul_f32 v[114:115], v[80:81], s[16:17] op_sel_hi:[1,0]
	v_pk_mul_f32 v[116:117], v[78:79], s[16:17] op_sel_hi:[1,0]
	v_pk_mul_f32 v[122:123], v[72:73], s[16:17] op_sel_hi:[1,0]
	v_pk_mul_f32 v[124:125], v[70:71], s[16:17] op_sel_hi:[1,0]
	v_pk_mul_f32 v[70:71], v[88:89], s[16:17] op_sel_hi:[1,0]
	v_pk_mul_f32 v[72:73], v[86:87], s[16:17] op_sel_hi:[1,0]
	v_pk_mul_f32 v[78:79], v[84:85], s[16:17] op_sel_hi:[1,0]
	v_pk_mul_f32 v[80:81], v[82:83], s[16:17] op_sel_hi:[1,0]
	v_pk_mul_f32 v[82:83], v[64:65], s[16:17] op_sel_hi:[1,0]
	v_pk_mul_f32 v[84:85], v[62:63], s[16:17] op_sel_hi:[1,0]
	v_pk_mul_f32 v[86:87], v[56:57], s[16:17] op_sel_hi:[1,0]
	v_pk_mul_f32 v[88:89], v[54:55], s[16:17] op_sel_hi:[1,0]
	v_pk_mul_f32 v[54:55], v[76:77], s[16:17] op_sel_hi:[1,0]
	v_pk_mul_f32 v[56:57], v[74:75], s[16:17] op_sel_hi:[1,0]
	v_pk_mul_f32 v[62:63], v[68:69], s[16:17] op_sel_hi:[1,0]
	v_pk_mul_f32 v[64:65], v[66:67], s[16:17] op_sel_hi:[1,0]
	v_pk_mul_f32 v[66:67], v[48:49], s[16:17] op_sel_hi:[1,0]
	v_pk_mul_f32 v[68:69], v[46:47], s[16:17] op_sel_hi:[1,0]
	v_pk_mul_f32 v[74:75], v[44:45], s[16:17] op_sel_hi:[1,0]
	v_pk_mul_f32 v[76:77], v[42:43], s[16:17] op_sel_hi:[1,0]
	v_pk_mul_f32 v[42:43], v[60:61], s[16:17] op_sel_hi:[1,0]
	v_pk_mul_f32 v[44:45], v[58:59], s[16:17] op_sel_hi:[1,0]
	v_pk_mul_f32 v[46:47], v[52:53], s[16:17] op_sel_hi:[1,0]
	v_pk_mul_f32 v[48:49], v[50:51], s[16:17] op_sel_hi:[1,0]
	v_pk_mul_f32 v[40:41], v[40:41], s[16:17] op_sel_hi:[1,0]
	v_pk_mul_f32 v[38:39], v[38:39], s[16:17] op_sel_hi:[1,0]
	v_pk_mul_f32 v[36:37], v[36:37], s[16:17] op_sel_hi:[1,0]
	v_pk_mul_f32 v[34:35], v[34:35], s[16:17] op_sel_hi:[1,0]

; #define LAS __attribute__((address_space(3)))
; __device__ __forceinline__ void phase6(const Args& a, LAS unsigned char* lds, int tid, int lane, int wave, int vcu, int G) {
;     unsigned char* ws = a.ws;
;     const float* mod = (const float*)(ws + WS_MOD); const bf16* Y1 = (const bf16*)(ws + RA_Y1); bf16* X1 = (bf16*)(ws + RA_X1); unsigned char* H2 = ws + RA_H2;
;     const float* gpost = a.in[7]; const float* gpre2 = a.in[8]; const float* rbias = a.in[20];
;     const bf16* whi = (const bf16*)(ws + WS_WRT);
;     LAS float* part = (LAS float*)lds;
;     LAS float* logit = (LAS float*)(lds + LDS_LOGIT);
;     LAS u64* masks = (LAS u64*)(lds + LDS_MASKS);
;     int* cnt = (int*)(ws + T_CNT); u64* tmask = (u64*)(ws + T_MASK); float* tokw = (float*)(ws + T_TOKW);
;     const int l15 = lane & 15, l4 = lane >> 4;
;     const float rb = rbias[lane];
;     for (int blk = vcu; blk < NT / 64; blk += G) {
.LBB0_1080:
	s_setprio 0
	s_cmp_gt_i32 s94, 7
	s_cselect_b64 s[0:1], -1, 0
	s_cmp_lt_i32 s95, 8
	s_cselect_b64 s[2:3], -1, 0
	s_or_b64 s[0:1], s[0:1], s[2:3]
	s_and_b64 vcc, exec, s[0:1]
	s_cbranch_vccnz .LBB0_1152
	v_mov_b32_e32 v2, v0
	v_readlane_b32 s0, v246, 2
	s_cmpk_gt_i32 s0, 0xff
	v_readfirstlane_b32 s2, v2
	s_cbranch_scc1 .LBB0_1102
	v_and_b32_e32 v14, 63, v2
	v_lshlrev_b32_e32 v16, 2, v14
	global_load_dword v15, v16, s[60:61]
	s_add_u32 s33, s92, 0x100000
	s_addc_u32 s38, s93, 0
	s_add_u32 s30, s92, 0x39c00000
	s_addc_u32 s31, s93, 0
	s_add_u32 s39, s92, 0x39c10000
	s_addc_u32 s40, s93, 0
	s_add_u32 s41, s92, 0x39c30000
	s_addc_u32 s44, s93, 0
	s_ashr_i32 s24, s2, 6
	v_bfe_u32 v1, v2, 4, 2
	s_lshl_b32 s0, s24, 9
	s_lshl_b32 s45, s24, 2
	v_lshlrev_b32_e32 v4, 3, v1
	s_add_i32 s0, s0, 0
	s_add_i32 s4, 0, 0x20200
	v_mov_b32_e32 v17, 0
	v_lshl_or_b32 v4, s24, 8, v4
	v_and_b32_e32 v5, 48, v2
	v_lshlrev_b64 v[6:7], v2, -1
	s_cmp_lt_u32 s2, 64
	v_readlane_b32 s8, v246, 3
	v_and_b32_e32 v3, 15, v2
	v_add_u32_e32 v11, s0, v5
	v_not_b32_e32 v20, v6
	s_cselect_b64 s[42:43], -1, 0
	s_add_i32 s2, 0, 0x22200
	v_lshlrev_b32_e32 v6, 3, v14
	v_lshlrev_b32_e32 v8, 4, v14
	v_mov_b32_e32 v9, v17
	v_readlane_b32 s9, v246, 4
	v_or_b32_e32 v102, 0x400, v16
	v_ashrrev_i32_e32 v5, 31, v4
	v_add_u32_e32 v99, s2, v6
	v_lshl_add_u64 v[22:23], s[8:9], 0, v[8:9]
	s_waitcnt lgkmcnt(0)
	v_lshl_add_u64 v[24:25], s[82:83], 0, v[8:9]
	v_lshlrev_b32_e32 v8, 2, v102
	v_lshl_add_u64 v[4:5], v[4:5], 1, s[92:93]
	s_mov_b64 s[2:3], 0x180000
	v_lshlrev_b32_e32 v48, 12, v3
	v_lshl_add_u64 v[26:27], s[82:83], 0, v[8:9]
	v_lshl_add_u64 v[34:35], s[8:9], 0, v[8:9]
	v_lshl_add_u64 v[8:9], v[4:5], 0, s[2:3]
	v_mov_b32_e32 v49, v17
	v_or_b32_e32 v86, 0x10000, v48
	v_mov_b32_e32 v87, v17
	v_or_b32_e32 v88, 0x20000, v48
	v_mov_b32_e32 v89, v17
	v_or_b32_e32 v90, 0x30000, v48
	v_mov_b32_e32 v91, v17
	s_mov_b64 s[2:3], 0x180040
	v_lshl_add_u64 v[42:43], v[8:9], 0, v[48:49]
	v_lshl_add_u64 v[44:45], v[8:9], 0, v[86:87]
	v_lshl_add_u64 v[46:47], v[8:9], 0, v[88:89]
	v_lshl_add_u64 v[48:49], v[8:9], 0, v[90:91]
	v_lshl_add_u64 v[8:9], v[4:5], 0, s[2:3]
	s_mov_b64 s[2:3], 0x180080
	v_lshl_add_u64 v[50:51], v[8:9], 0, v[86:87]
	v_lshl_add_u64 v[52:53], v[8:9], 0, v[88:89]
	v_lshl_add_u64 v[54:55], v[8:9], 0, v[90:91]
	v_lshl_add_u64 v[8:9], v[4:5], 0, s[2:3]
	s_mov_b64 s[2:3], 0x1800c0
	v_lshl_add_u64 v[56:57], v[8:9], 0, v[86:87]
	v_lshl_add_u64 v[58:59], v[8:9], 0, v[88:89]
	v_lshl_add_u64 v[60:61], v[8:9], 0, v[90:91]
	v_lshl_add_u64 v[8:9], v[4:5], 0, s[2:3]
	s_mov_b64 s[2:3], 0x180100
	v_lshl_add_u64 v[62:63], v[8:9], 0, v[86:87]
	v_lshl_add_u64 v[64:65], v[8:9], 0, v[88:89]
	v_lshl_add_u64 v[66:67], v[8:9], 0, v[90:91]
	v_lshl_add_u64 v[8:9], v[4:5], 0, s[2:3]
	s_mov_b64 s[2:3], 0x180140
	v_lshl_add_u64 v[68:69], v[8:9], 0, v[86:87]
	v_lshl_add_u64 v[70:71], v[8:9], 0, v[88:89]
	v_lshl_add_u64 v[72:73], v[8:9], 0, v[90:91]
	v_lshl_add_u64 v[8:9], v[4:5], 0, s[2:3]
	s_mov_b64 s[2:3], 0x180180
	v_lshl_add_u64 v[74:75], v[8:9], 0, v[86:87]
	v_lshl_add_u64 v[76:77], v[8:9], 0, v[88:89]
	v_lshl_add_u64 v[78:79], v[8:9], 0, v[90:91]
	v_lshl_add_u64 v[8:9], v[4:5], 0, s[2:3]
	s_mov_b64 s[2:3], 0x1801c0
	v_lshlrev_b32_e32 v1, 10, v1
	v_lshl_add_u64 v[4:5], v[4:5], 0, s[2:3]
	v_lshl_or_b32 v13, s24, 13, v1
	v_and_b32_e32 v18, 56, v2
	v_and_b32_e32 v21, 7, v2
	v_not_b32_e32 v1, v7
	v_readlane_b32 s16, v246, 11
	v_readlane_b32 s17, v246, 12
	v_lshl_add_u64 v[80:81], v[8:9], 0, v[86:87]
	v_lshl_add_u64 v[82:83], v[8:9], 0, v[88:89]
	v_lshl_add_u64 v[84:85], v[8:9], 0, v[90:91]
	v_lshl_add_u64 v[86:87], v[4:5], 0, v[86:87]
	v_lshl_add_u64 v[88:89], v[4:5], 0, v[88:89]
	v_lshl_add_u64 v[90:91], v[4:5], 0, v[90:91]
	s_movk_i32 s2, 0x1010
	v_mov_b32_e32 v5, 0x10100
	v_lshlrev_b32_e32 v2, 2, v2
	v_mov_b32_e32 v7, v17
	v_lshl_add_u32 v101, v3, 2, 0
	v_mul_u32_u24_e32 v4, 0x1010, v3
	v_mad_u32_u24 v5, v3, s2, v5
	v_add_u32_e32 v122, 0, v2
	v_add_u32_e32 v123, s4, v2
	v_lshl_add_u64 v[2:3], s[92:93], 0, v[6:7]
	s_mov_b64 s[16:17], 0x22200000
	v_readlane_b32 s18, v246, 13
	v_lshl_add_u64 v[92:93], v[2:3], 0, s[16:17]
	s_mov_b64 s[16:17], 0x26200000
	v_lshl_add_u64 v[94:95], v[2:3], 0, s[16:17]
	v_lshl_add_u64 v[2:3], s[92:93], 0, v[16:17]
	s_mov_b64 s[16:17], 0x1a200000
	s_mul_i32 s18, s24, 0x4040
	v_or_b32_e32 v104, 0x500, v16
	v_or_b32_e32 v106, 0x600, v16
	v_or_b32_e32 v108, 0x700, v16
	v_lshl_add_u64 v[96:97], v[2:3], 0, s[16:17]
	s_add_i32 s16, s18, 0
	v_readlane_b32 s51, v246, 2
	v_readlane_b32 s10, v246, 5
	v_readlane_b32 s11, v246, 6
	v_readlane_b32 s12, v246, 7
	v_readlane_b32 s13, v246, 8
	v_readlane_b32 s14, v246, 9
	v_readlane_b32 s15, v246, 10
	v_or_b32_e32 v10, 0x100, v16
	v_or_b32_e32 v12, 0x200, v16
	v_or_b32_e32 v100, 0x300, v16
	v_lshlrev_b32_e32 v36, 2, v104
	v_mov_b32_e32 v37, v17
	v_lshlrev_b32_e32 v38, 2, v106
	v_mov_b32_e32 v39, v17
	v_lshlrev_b32_e32 v40, 2, v108
	v_mov_b32_e32 v41, v17
	v_add_u32_e32 v127, s16, v6
	s_lshl_b32 s16, s51, 6
	s_mov_b32 s35, 0
	v_add_u32_e32 v19, s4, v16
	v_cmp_eq_u32_e64 s[0:1], 0, v14
	v_lshl_add_u64 v[28:29], s[82:83], 0, v[36:37]
	v_lshl_add_u64 v[30:31], s[82:83], 0, v[38:39]
	v_lshl_add_u64 v[32:33], s[82:83], 0, v[40:41]
	v_lshl_add_u64 v[36:37], s[8:9], 0, v[36:37]
	v_lshl_add_u64 v[38:39], s[8:9], 0, v[38:39]
	v_lshl_add_u64 v[40:41], s[8:9], 0, v[40:41]
	v_add_u32_e32 v124, 0x800, v123
	v_add_u32_e32 v125, 0x1000, v123
	v_add_u32_e32 v126, 0x1800, v123
	v_cmp_lt_u32_e64 s[2:3], 7, v14
	v_cmp_lt_u32_e64 s[4:5], 15, v14
	v_cmp_lt_u32_e64 s[6:7], 23, v14
	v_cmp_lt_u32_e64 s[8:9], 31, v14
	v_cmp_lt_u32_e64 s[10:11], 39, v14
	v_cmp_lt_u32_e64 s[12:13], 47, v14
	v_cmp_eq_u32_e64 s[14:15], 56, v18
	s_add_i32 s46, s16, s45
	s_lshl_b32 s47, s97, 6
	v_sub_u32_e32 v98, 0, v14
	v_lshlrev_b32_e32 v128, 2, v16
	v_lshlrev_b32_e32 v129, 2, v102
	v_lshlrev_b32_e32 v130, 2, v104
	v_lshlrev_b32_e32 v131, 2, v106
	v_lshlrev_b32_e32 v132, 2, v108
	v_mov_b32_e32 v133, 0x358637bd
	s_mov_b32 s48, 0x800000
	s_movk_i32 s49, 0x7fff
	v_lshlrev_b32_e32 v134, 2, v10
	v_lshlrev_b32_e32 v135, 2, v12
	v_lshlrev_b32_e32 v136, 2, v100
	s_mov_b32 s50, 0xc3e00000
	v_add_u32_e32 v137, v11, v4
	v_add_u32_e32 v138, v11, v5
	v_add_u32_e32 v139, v101, v13
	v_mov_b32_e32 v140, 0x3a000000
	v_mov_b32_e32 v141, 1
	v_mov_b32_e32 v142, 0x43e00000
	v_mov_b32_e32 v143, 0xff800000
	v_readlane_b32 s19, v246, 14
	v_readlane_b32 s20, v246, 15
	v_readlane_b32 s21, v246, 16
	v_readlane_b32 s22, v246, 17
	v_readlane_b32 s23, v246, 18
	s_branch .LBB0_1084

; #define PG8_STAGE(bufoff, gbase, v0, v1) do { \
;         __builtin_amdgcn_global_load_lds((const unsigned*)((const char*)(gbase) + (v0)), (LAS unsigned*)(lds + (bufoff) + ldsw), 16, 0, 0); \
;         __builtin_amdgcn_global_load_lds((const unsigned*)((const char*)(gbase) + (v1)), (LAS unsigned*)(lds + (bufoff) + ldsw + 8192), 16, 0, 0); } while (0)
; #define PG8_LDA(dst, b, h) do { _Pragma("unroll") for (int m = 0; m < 4; ++m) { const v4i lo_ = *(const LAS v4i*)(lds + PG8_SA(b, h) + aoff + m * 2048), hi_ = *(const LAS v4i*)(lds + PG8_SA(b, h) + aoff + m * 2048 + 1024); \
;         dst[m] = __builtin_shufflevector(lo_, hi_, 0, 1, 2, 3, 4, 5, 6, 7); } } while (0)
; #define PG8_LDB(dst, b, h) do { _Pragma("unroll") for (int n = 0; n < 2; ++n) { const v4i lo_ = *(const LAS v4i*)(lds + PG8_SB(b, h) + boff + n * 2048), hi_ = *(const LAS v4i*)(lds + PG8_SB(b, h) + boff + n * 2048 + 1024); \
;         dst[n] = __builtin_shufflevector(lo_, hi_, 0, 1, 2, 3, 4, 5, 6, 7); } } while (0)
; #define PG8_WAIT_V(n) asm volatile("s_waitcnt vmcnt(" #n ")" ::: "memory")
; #define PG8_WAIT_L(n) asm volatile("s_waitcnt lgkmcnt(" #n ")" ::: "memory")
; #define PG8_BAR __builtin_amdgcn_s_barrier()
; #define PG8_SCHED __builtin_amdgcn_sched_barrier(0)
; template <class Epi, class Sched, bool FP8 = false>
; __device__ __forceinline__ void gemm_phase(LAS unsigned char* lds, const int K, const Sched& S, const Epi& E) {
;     ...
;             PG8_LDB(B0, 0, 0); PG8_LDB(B1, 0, 1); PG8_SCHED; PG8_LDA(At, 0, 0); PG8_STAGE(PG8_SA(1, 1), a1, vA[2], vA[3]);
;             PG8_WAIT_V(8); PG8_WAIT_L(0); PG8_BAR; PG8_MMA(0, 0, At, B0); PG8_MMA(0, 1, At, B1); PG8_BAR; PG8_SCHED;
;             PG8_LDA(At, 0, 1); PG8_STAGE(PG8_SB(0, 0), b2, voffB[0], voffB[1]); PG8_STAGE(PG8_SB(0, 1), b2 + hstepB, voffB[0], voffB[1]); PG8_STAGE(PG8_SA(0, 0), a2, x0, x1);
;             PG8_WAIT_V(8); PG8_WAIT_L(0); PG8_BAR; if (!lo_only) { PG8_MMA(1, 0, At, B0); PG8_MMA(1, 1, At, B1); } PG8_BAR; PG8_SCHED;
;             PG8_LDB(B0, 1, 0); PG8_LDB(B1, 1, 1); PG8_SCHED; PG8_LDA(At, 1, 0); PG8_STAGE(PG8_SA(0, 1), a2, x2, x3);
.LBB0_1294:
	ds_read_b128 v[18:21], v228
	ds_read_b128 v[22:25], v228 offset:1024
	ds_read_b128 v[26:29], v228 offset:2048
	ds_read_b128 v[30:33], v228 offset:3072
	ds_read_b128 v[2:5], v229
	ds_read_b128 v[6:9], v229 offset:1024
	ds_read_b128 v[10:13], v229 offset:2048
	ds_read_b128 v[14:17], v229 offset:3072
	s_cmp_eq_u32 s55, s68
	s_cselect_b64 s[6:7], -1, 0
	s_add_u32 s8, s34, s40
	s_addc_u32 s9, s35, s41
	s_add_u32 s42, s8, 0x100
	s_addc_u32 s43, s9, 0
	s_and_b64 s[8:9], s[6:7], exec
	s_cselect_b32 s43, s37, s43
	s_cselect_b32 s42, s36, s42
	s_add_u32 s69, s66, s40
	s_addc_u32 s70, s67, s41
	s_and_b64 s[8:9], s[6:7], exec
	v_cndmask_b32_e64 v66, v206, v234, s[6:7]
	s_cselect_b32 s9, s31, s70
	s_cselect_b32 s8, s30, s69
	v_cndmask_b32_e64 v68, v204, v235, s[6:7]
	s_mov_b32 m0, s58
	v_lshl_add_u64 v[214:215], v[210:211], 0, s[40:41]
	s_waitcnt lgkmcnt(0)
	ds_read_b128 v[34:37], v230
	ds_read_b128 v[38:41], v230 offset:1024
	ds_read_b128 v[42:45], v230 offset:2048
	ds_read_b128 v[46:49], v230 offset:3072
	ds_read_b128 v[50:53], v230 offset:4096
	ds_read_b128 v[54:57], v230 offset:5120
	ds_read_b128 v[58:61], v230 offset:6144
	ds_read_b128 v[62:65], v230 offset:7168
	global_load_lds_dwordx4 v[214:215], off
	v_lshl_add_u64 v[214:215], v[212:213], 0, s[40:41]
	s_mov_b32 m0, s59
	s_nop 0
	global_load_lds_dwordx4 v[214:215], off
	s_waitcnt vmcnt(8)
	s_waitcnt lgkmcnt(0)
	s_barrier
	s_nop 4
	s_waitcnt lgkmcnt(0)
	v_mfma_f32_16x16x128_f8f6f4 v[186:189], v[18:25], v[34:41], v[186:189]
	v_mfma_f32_16x16x128_f8f6f4 v[182:185], v[26:33], v[34:41], v[182:185]
	v_mfma_f32_16x16x128_f8f6f4 v[170:173], v[18:25], v[42:49], v[170:173]
	v_mfma_f32_16x16x128_f8f6f4 v[166:169], v[26:33], v[42:49], v[166:169]
	v_mfma_f32_16x16x128_f8f6f4 v[154:157], v[18:25], v[50:57], v[154:157]
	v_mfma_f32_16x16x128_f8f6f4 v[150:153], v[26:33], v[50:57], v[150:153]
	v_mfma_f32_16x16x128_f8f6f4 v[138:141], v[18:25], v[58:65], v[138:141]
	v_mfma_f32_16x16x128_f8f6f4 v[134:137], v[26:33], v[58:65], v[134:137]
	s_nop 4
	v_mfma_f32_16x16x128_f8f6f4 v[194:197], v[2:9], v[34:41], v[194:197]
	v_mfma_f32_16x16x128_f8f6f4 v[190:193], v[10:17], v[34:41], v[190:193]
	v_mfma_f32_16x16x128_f8f6f4 v[178:181], v[2:9], v[42:49], v[178:181]
	v_mfma_f32_16x16x128_f8f6f4 v[174:177], v[10:17], v[42:49], v[174:177]
	v_mfma_f32_16x16x128_f8f6f4 v[162:165], v[2:9], v[50:57], v[162:165]
	v_mfma_f32_16x16x128_f8f6f4 v[158:161], v[10:17], v[50:57], v[158:161]
	v_mfma_f32_16x16x128_f8f6f4 v[146:149], v[2:9], v[58:65], v[146:149]
	v_mfma_f32_16x16x128_f8f6f4 v[142:145], v[10:17], v[58:65], v[142:145]
	s_barrier
	s_mov_b32 m0, s60
	v_lshl_add_u64 v[216:217], s[8:9], 0, v[198:199]
	v_lshl_add_u64 v[214:215], s[8:9], 0, v[200:201]
	s_add_u32 s8, s8, s16
	ds_read_b128 v[58:61], v230 offset:16384
	ds_read_b128 v[62:65], v230 offset:17408
	ds_read_b128 v[50:53], v230 offset:18432
	ds_read_b128 v[54:57], v230 offset:19456
	ds_read_b128 v[42:45], v230 offset:20480
	ds_read_b128 v[46:49], v230 offset:21504
	ds_read_b128 v[34:37], v230 offset:22528
	ds_read_b128 v[38:41], v230 offset:23552
	global_load_lds_dwordx4 v[216:217], off
	s_mov_b32 m0, s61
	s_addc_u32 s9, s9, s17
	global_load_lds_dwordx4 v[214:215], off
	v_lshl_add_u64 v[220:221], s[8:9], 0, v[198:199]
	s_mov_b32 m0, s62
	v_lshl_add_u64 v[218:219], s[8:9], 0, v[200:201]
	global_load_lds_dwordx4 v[220:221], off
	s_mov_b32 m0, s63
	v_cmp_ne_u32_e64 s[8:9], 1, v203
	global_load_lds_dwordx4 v[218:219], off
	s_mov_b32 m0, s46
	s_andn2_b64 vcc, exec, s[4:5]
	global_load_lds_dwordx4 v66, s[42:43]
	s_mov_b32 m0, s47
	s_nop 0
	global_load_lds_dwordx4 v68, s[42:43]
	s_waitcnt vmcnt(8)
	s_waitcnt lgkmcnt(0)
	s_barrier
	s_cbranch_vccnz .LBB0_1296
	s_nop 4
	s_waitcnt lgkmcnt(0)
	v_mfma_f32_16x16x128_f8f6f4 v[122:125], v[18:25], v[58:65], v[122:125]
	v_mfma_f32_16x16x128_f8f6f4 v[118:121], v[26:33], v[58:65], v[118:121]
	v_mfma_f32_16x16x128_f8f6f4 v[106:109], v[18:25], v[50:57], v[106:109]
	v_mfma_f32_16x16x128_f8f6f4 v[102:105], v[26:33], v[50:57], v[102:105]
	v_mfma_f32_16x16x128_f8f6f4 v[90:93], v[18:25], v[42:49], v[90:93]
	v_mfma_f32_16x16x128_f8f6f4 v[86:89], v[26:33], v[42:49], v[86:89]
	v_mfma_f32_16x16x128_f8f6f4 v[74:77], v[18:25], v[34:41], v[74:77]
	v_mfma_f32_16x16x128_f8f6f4 v[70:73], v[26:33], v[34:41], v[70:73]
	s_nop 4
	v_mfma_f32_16x16x128_f8f6f4 v[130:133], v[2:9], v[58:65], v[130:133]
	v_mfma_f32_16x16x128_f8f6f4 v[126:129], v[10:17], v[58:65], v[126:129]
	v_mfma_f32_16x16x128_f8f6f4 v[114:117], v[2:9], v[50:57], v[114:117]
	v_mfma_f32_16x16x128_f8f6f4 v[110:113], v[10:17], v[50:57], v[110:113]
	v_mfma_f32_16x16x128_f8f6f4 v[98:101], v[2:9], v[42:49], v[98:101]
	v_mfma_f32_16x16x128_f8f6f4 v[94:97], v[10:17], v[42:49], v[94:97]
	v_mfma_f32_16x16x128_f8f6f4 v[82:85], v[2:9], v[34:41], v[82:85]
	v_mfma_f32_16x16x128_f8f6f4 v[78:81], v[10:17], v[34:41], v[78:81]
; #define PG8_STAGE(bufoff, gbase, v0, v1) do { \
;         __builtin_amdgcn_global_load_lds((const unsigned*)((const char*)(gbase) + (v0)), (LAS unsigned*)(lds + (bufoff) + ldsw), 16, 0, 0); \
;         __builtin_amdgcn_global_load_lds((const unsigned*)((const char*)(gbase) + (v1)), (LAS unsigned*)(lds + (bufoff) + ldsw + 8192), 16, 0, 0); } while (0)
; #define PG8_LDA(dst, b, h) do { _Pragma("unroll") for (int m = 0; m < 4; ++m) { const v4i lo_ = *(const LAS v4i*)(lds + PG8_SA(b, h) + aoff + m * 2048), hi_ = *(const LAS v4i*)(lds + PG8_SA(b, h) + aoff + m * 2048 + 1024); \
;         dst[m] = __builtin_shufflevector(lo_, hi_, 0, 1, 2, 3, 4, 5, 6, 7); } } while (0)
; #define PG8_WAIT_V(n) asm volatile("s_waitcnt vmcnt(" #n ")" ::: "memory")
; #define PG8_WAIT_L(n) asm volatile("s_waitcnt lgkmcnt(" #n ")" ::: "memory")
; #define PG8_BAR __builtin_amdgcn_s_barrier()
; #define PG8_SCHED __builtin_amdgcn_sched_barrier(0)
; template <class Epi, class Sched, bool FP8 = false>
; __device__ __forceinline__ void gemm_phase(LAS unsigned char* lds, const int K, const Sched& S, const Epi& E) {
;     ...
;             PG8_LDA(At, 0, 1); PG8_STAGE(PG8_SB(0, 0), b2, voffB[0], voffB[1]); PG8_STAGE(PG8_SB(0, 1), b2 + hstepB, voffB[0], voffB[1]); PG8_STAGE(PG8_SA(0, 0), a2, x0, x1);
;             PG8_WAIT_V(8); PG8_WAIT_L(0); PG8_BAR; if (!lo_only) { PG8_MMA(1, 0, At, B0); PG8_MMA(1, 1, At, B1); } PG8_BAR; PG8_SCHED;
;             PG8_LDB(B0, 1, 0); PG8_LDB(B1, 1, 1); PG8_SCHED; PG8_LDA(At, 1, 0); PG8_STAGE(PG8_SA(0, 1), a2, x2, x3);
;             PG8_WAIT_V(8); PG8_WAIT_L(0); PG8_BAR; PG8_MMA(0, 0, At, B0); PG8_MMA(0, 1, At, B1); PG8_BAR; PG8_SCHED;
;             PG8_LDA(At, 1, 1); PG8_STAGE(PG8_SB(1, 0), b3, voffB[0], voffB[1]); PG8_STAGE(PG8_SB(1, 1), b3 + hstepB, voffB[0], voffB[1]); PG8_STAGE(PG8_SA(1, 0), a3, x0, x1);
;             PG8_WAIT_V(8); PG8_WAIT_L(0); PG8_BAR; if (!lo_only) { PG8_MMA(1, 0, At, B0); PG8_MMA(1, 1, At, B1); } PG8_BAR; PG8_SCHED;
;     __device__ __forceinline__ void aoffs(const U& u, const int (&R)[2], const int (&C)[2], unsigned (&v)[4]) const {
; #pragma unroll
;         for (int h = 0; h < 2; ++h)
; #pragma unroll
;             for (int i = 0; i < 2; ++i) { int r = h * 128 + R[i]; r = r < u.nrows ? r : u.nrows - 1; const int tok = slot_tok[u.row0 + r]; v[h * 2 + i] = (unsigned)(tok * 1024 + C[i]) * 2u; }
;     }
.LBB0_1296:
	v_lshl_or_b32 v234, v240, 11, v225
	v_lshl_or_b32 v235, v241, 11, v225
	v_lshl_or_b32 v236, v242, 11, v225
	v_lshl_or_b32 v237, v243, 11, v225
	v_mov_b32_e32 v69, v67
	v_lshl_add_u64 v[238:239], s[42:43], 0, v[66:67]
	v_lshl_add_u64 v[68:69], s[42:43], 0, v[68:69]
	v_cndmask_b32_e64 v66, v202, v236, s[6:7]
	v_cndmask_b32_e64 v209, v208, v237, s[6:7]
	s_barrier
	s_add_i32 s6, 0, 0x18000
	s_add_i32 s7, 0, 0x1c000
	v_add_u32_e32 v2, s6, v205
	v_add_u32_e32 v14, s7, v205
	ds_read_b128 v[18:21], v2
	ds_read_b128 v[22:25], v2 offset:1024
	ds_read_b128 v[26:29], v2 offset:2048
	ds_read_b128 v[30:33], v2 offset:3072
	ds_read_b128 v[2:5], v14
	ds_read_b128 v[6:9], v14 offset:1024
	ds_read_b128 v[10:13], v14 offset:2048
	ds_read_b128 v[14:17], v14 offset:3072
	s_mov_b32 m0, s48
	s_waitcnt lgkmcnt(0)
	ds_read_b128 v[34:37], v230 offset:32768
	ds_read_b128 v[38:41], v230 offset:33792
	ds_read_b128 v[42:45], v230 offset:34816
	ds_read_b128 v[46:49], v230 offset:35840
	ds_read_b128 v[50:53], v230 offset:36864
	ds_read_b128 v[54:57], v230 offset:37888
	ds_read_b128 v[58:61], v230 offset:38912
	ds_read_b128 v[62:65], v230 offset:39936
	global_load_lds_dwordx4 v66, s[42:43]
	s_mov_b32 m0, s49
	s_nop 0
	global_load_lds_dwordx4 v209, s[42:43]
	s_waitcnt vmcnt(8)
	s_waitcnt lgkmcnt(0)
	s_barrier
	s_nop 4
	s_waitcnt lgkmcnt(0)
	v_mfma_f32_16x16x128_f8f6f4 v[186:189], v[18:25], v[34:41], v[186:189]
	v_mfma_f32_16x16x128_f8f6f4 v[182:185], v[26:33], v[34:41], v[182:185]
	v_mfma_f32_16x16x128_f8f6f4 v[170:173], v[18:25], v[42:49], v[170:173]
	v_mfma_f32_16x16x128_f8f6f4 v[166:169], v[26:33], v[42:49], v[166:169]
	v_mfma_f32_16x16x128_f8f6f4 v[154:157], v[18:25], v[50:57], v[154:157]
	v_mfma_f32_16x16x128_f8f6f4 v[150:153], v[26:33], v[50:57], v[150:153]
	v_mfma_f32_16x16x128_f8f6f4 v[138:141], v[18:25], v[58:65], v[138:141]
	v_mfma_f32_16x16x128_f8f6f4 v[134:137], v[26:33], v[58:65], v[134:137]
	s_nop 4
	v_mfma_f32_16x16x128_f8f6f4 v[194:197], v[2:9], v[34:41], v[194:197]
	v_mfma_f32_16x16x128_f8f6f4 v[190:193], v[10:17], v[34:41], v[190:193]
	v_mfma_f32_16x16x128_f8f6f4 v[178:181], v[2:9], v[42:49], v[178:181]
	v_mfma_f32_16x16x128_f8f6f4 v[174:177], v[10:17], v[42:49], v[174:177]
	v_mfma_f32_16x16x128_f8f6f4 v[162:165], v[2:9], v[50:57], v[162:165]
	v_mfma_f32_16x16x128_f8f6f4 v[158:161], v[10:17], v[50:57], v[158:161]
	v_mfma_f32_16x16x128_f8f6f4 v[146:149], v[2:9], v[58:65], v[146:149]
	v_mfma_f32_16x16x128_f8f6f4 v[142:145], v[10:17], v[58:65], v[142:145]
	s_barrier
	s_add_i32 s6, s6, s45
	v_lshl_add_u64 v[216:217], v[216:217], 0, s[24:25]
	s_mov_b32 m0, s6
	ds_read_b128 v[58:61], v230 offset:49152
	ds_read_b128 v[62:65], v230 offset:50176
	ds_read_b128 v[50:53], v230 offset:51200
	ds_read_b128 v[54:57], v230 offset:52224
	ds_read_b128 v[42:45], v230 offset:53248
	ds_read_b128 v[46:49], v230 offset:54272
	ds_read_b128 v[34:37], v230 offset:55296
	ds_read_b128 v[38:41], v230 offset:56320
	global_load_lds_dwordx4 v[216:217], off
	v_lshl_add_u64 v[214:215], v[214:215], 0, s[24:25]
	s_add_i32 m0, s6, 0x2000
	s_add_i32 s6, s7, s45
	global_load_lds_dwordx4 v[214:215], off
	v_lshl_add_u64 v[214:215], v[220:221], 0, s[24:25]
	s_mov_b32 m0, s6
	v_lshl_add_u64 v[68:69], v[68:69], 0, s[24:25]
	global_load_lds_dwordx4 v[214:215], off
	v_lshl_add_u64 v[214:215], v[218:219], 0, s[24:25]
	s_add_i32 m0, s6, 0x2000
	s_and_b64 vcc, exec, s[8:9]
	global_load_lds_dwordx4 v[214:215], off
	v_lshl_add_u64 v[214:215], v[238:239], 0, s[24:25]
	s_mov_b32 m0, s52
	s_nop 0
	global_load_lds_dwordx4 v[214:215], off
	s_mov_b32 m0, s53
	s_nop 0
	global_load_lds_dwordx4 v[68:69], off
	s_waitcnt vmcnt(8)
	s_waitcnt lgkmcnt(0)
	s_barrier
	s_cbranch_vccnz .LBB0_1293
	s_nop 4
	s_waitcnt lgkmcnt(0)
	v_mfma_f32_16x16x128_f8f6f4 v[122:125], v[18:25], v[58:65], v[122:125]
	v_mfma_f32_16x16x128_f8f6f4 v[118:121], v[26:33], v[58:65], v[118:121]
	v_mfma_f32_16x16x128_f8f6f4 v[106:109], v[18:25], v[50:57], v[106:109]
	v_mfma_f32_16x16x128_f8f6f4 v[102:105], v[26:33], v[50:57], v[102:105]
	v_mfma_f32_16x16x128_f8f6f4 v[90:93], v[18:25], v[42:49], v[90:93]
	v_mfma_f32_16x16x128_f8f6f4 v[86:89], v[26:33], v[42:49], v[86:89]
	v_mfma_f32_16x16x128_f8f6f4 v[74:77], v[18:25], v[34:41], v[74:77]
	v_mfma_f32_16x16x128_f8f6f4 v[70:73], v[26:33], v[34:41], v[70:73]
	s_nop 4
	v_mfma_f32_16x16x128_f8f6f4 v[130:133], v[2:9], v[58:65], v[130:133]
	v_mfma_f32_16x16x128_f8f6f4 v[126:129], v[10:17], v[58:65], v[126:129]
	v_mfma_f32_16x16x128_f8f6f4 v[114:117], v[2:9], v[50:57], v[114:117]
	v_mfma_f32_16x16x128_f8f6f4 v[110:113], v[10:17], v[50:57], v[110:113]
	v_mfma_f32_16x16x128_f8f6f4 v[98:101], v[2:9], v[42:49], v[98:101]
	v_mfma_f32_16x16x128_f8f6f4 v[94:97], v[10:17], v[42:49], v[94:97]
	v_mfma_f32_16x16x128_f8f6f4 v[82:85], v[2:9], v[34:41], v[82:85]
	v_mfma_f32_16x16x128_f8f6f4 v[78:81], v[10:17], v[34:41], v[78:81]
	s_branch .LBB0_1293

; #define PG8_STAGE(bufoff, gbase, v0, v1) do { \
;         __builtin_amdgcn_global_load_lds((const unsigned*)((const char*)(gbase) + (v0)), (LAS unsigned*)(lds + (bufoff) + ldsw), 16, 0, 0); \
;         __builtin_amdgcn_global_load_lds((const unsigned*)((const char*)(gbase) + (v1)), (LAS unsigned*)(lds + (bufoff) + ldsw + 8192), 16, 0, 0); } while (0)
; #define PG8_LDA(dst, b, h) do { _Pragma("unroll") for (int m = 0; m < 4; ++m) { const v4i lo_ = *(const LAS v4i*)(lds + PG8_SA(b, h) + aoff + m * 2048), hi_ = *(const LAS v4i*)(lds + PG8_SA(b, h) + aoff + m * 2048 + 1024); \
;         dst[m] = __builtin_shufflevector(lo_, hi_, 0, 1, 2, 3, 4, 5, 6, 7); } } while (0)
; #define PG8_LDB(dst, b, h) do { _Pragma("unroll") for (int n = 0; n < 2; ++n) { const v4i lo_ = *(const LAS v4i*)(lds + PG8_SB(b, h) + boff + n * 2048), hi_ = *(const LAS v4i*)(lds + PG8_SB(b, h) + boff + n * 2048 + 1024); \
;         dst[n] = __builtin_shufflevector(lo_, hi_, 0, 1, 2, 3, 4, 5, 6, 7); } } while (0)
; #define PG8_WAIT_V(n) asm volatile("s_waitcnt vmcnt(" #n ")" ::: "memory")
; #define PG8_WAIT_L(n) asm volatile("s_waitcnt lgkmcnt(" #n ")" ::: "memory")
; #define PG8_BAR __builtin_amdgcn_s_barrier()
; #define PG8_SCHED __builtin_amdgcn_sched_barrier(0)
; template <class Epi, class Sched, bool FP8 = false>
; __device__ __forceinline__ void gemm_phase(LAS unsigned char* lds, const int K, const Sched& S, const Epi& E) {
;     ...
;             PG8_LDB(B0, 0, 0); PG8_LDB(B1, 0, 1); PG8_SCHED; PG8_LDA(At, 0, 0); PG8_STAGE(PG8_SA(1, 1), a1, vA[2], vA[3]);
;             PG8_WAIT_V(8); PG8_WAIT_L(0); PG8_BAR; PG8_MMA(0, 0, At, B0); PG8_MMA(0, 1, At, B1); PG8_BAR; PG8_SCHED;
;             PG8_LDA(At, 0, 1); PG8_STAGE(PG8_SB(0, 0), b2, voffB[0], voffB[1]); PG8_STAGE(PG8_SB(0, 1), b2 + hstepB, voffB[0], voffB[1]); PG8_STAGE(PG8_SA(0, 0), a2, x0, x1);
;             PG8_WAIT_V(8); PG8_WAIT_L(0); PG8_BAR; if (!lo_only) { PG8_MMA(1, 0, At, B0); PG8_MMA(1, 1, At, B1); } PG8_BAR; PG8_SCHED;
;             PG8_LDB(B0, 1, 0); PG8_LDB(B1, 1, 1); PG8_SCHED; PG8_LDA(At, 1, 0); PG8_STAGE(PG8_SA(0, 1), a2, x2, x3);
.LBB0_1385:
	ds_read_b128 v[18:21], v235
	ds_read_b128 v[22:25], v235 offset:1024
	ds_read_b128 v[26:29], v235 offset:2048
	ds_read_b128 v[30:33], v235 offset:3072
	ds_read_b128 v[2:5], v236
	ds_read_b128 v[6:9], v236 offset:1024
	ds_read_b128 v[10:13], v236 offset:2048
	ds_read_b128 v[14:17], v236 offset:3072
	v_mov_b64_e32 v[222:223], v[220:221]
	s_cmp_eq_u32 s41, s57
	v_lshl_add_u64 v[220:221], v[222:223], 0, s[18:19]
	s_cselect_b64 vcc, -1, 0
	v_cndmask_b32_e32 v69, v221, v219, vcc
	v_cndmask_b32_e32 v68, v220, v218, vcc
	s_cselect_b32 s27, s23, s56
	s_cselect_b32 s26, s22, s55
	s_mov_b32 m0, s43
	v_lshl_add_u64 v[224:225], v[222:223], 0, v[212:213]
	s_waitcnt lgkmcnt(0)
	ds_read_b128 v[34:37], v237
	ds_read_b128 v[38:41], v237 offset:1024
	ds_read_b128 v[42:45], v237 offset:2048
	ds_read_b128 v[46:49], v237 offset:3072
	ds_read_b128 v[50:53], v237 offset:4096
	ds_read_b128 v[54:57], v237 offset:5120
	ds_read_b128 v[58:61], v237 offset:6144
	ds_read_b128 v[62:65], v237 offset:7168
	global_load_lds_dwordx4 v[224:225], off
	v_lshl_add_u64 v[222:223], v[222:223], 0, v[214:215]
	s_mov_b32 m0, s44
	s_nop 0
	global_load_lds_dwordx4 v[222:223], off
	s_waitcnt vmcnt(8)
	s_waitcnt lgkmcnt(0)
	s_barrier
	s_nop 4
	s_waitcnt lgkmcnt(0)
	v_mfma_f32_16x16x128_f8f6f4 v[194:197], v[18:25], v[34:41], v[194:197]
	v_mfma_f32_16x16x128_f8f6f4 v[190:193], v[26:33], v[34:41], v[190:193]
	v_mfma_f32_16x16x128_f8f6f4 v[186:189], v[18:25], v[42:49], v[186:189]
	v_mfma_f32_16x16x128_f8f6f4 v[182:185], v[26:33], v[42:49], v[182:185]
	v_mfma_f32_16x16x128_f8f6f4 v[174:177], v[18:25], v[50:57], v[174:177]
	v_mfma_f32_16x16x128_f8f6f4 v[166:169], v[26:33], v[50:57], v[166:169]
	v_mfma_f32_16x16x128_f8f6f4 v[158:161], v[18:25], v[58:65], v[158:161]
	v_mfma_f32_16x16x128_f8f6f4 v[150:153], v[26:33], v[58:65], v[150:153]
	s_nop 4
	v_mfma_f32_16x16x128_f8f6f4 v[178:181], v[2:9], v[34:41], v[178:181]
	v_mfma_f32_16x16x128_f8f6f4 v[170:173], v[10:17], v[34:41], v[170:173]
	v_mfma_f32_16x16x128_f8f6f4 v[162:165], v[2:9], v[42:49], v[162:165]
	v_mfma_f32_16x16x128_f8f6f4 v[154:157], v[10:17], v[42:49], v[154:157]
	v_mfma_f32_16x16x128_f8f6f4 v[146:149], v[2:9], v[50:57], v[146:149]
	v_mfma_f32_16x16x128_f8f6f4 v[142:145], v[10:17], v[50:57], v[142:145]
	v_mfma_f32_16x16x128_f8f6f4 v[138:141], v[2:9], v[58:65], v[138:141]
	v_mfma_f32_16x16x128_f8f6f4 v[122:125], v[10:17], v[58:65], v[122:125]
	s_barrier
	s_mov_b32 m0, s45
	v_lshl_add_u64 v[224:225], s[26:27], 0, v[200:201]
	v_lshl_add_u64 v[222:223], s[26:27], 0, v[202:203]
	s_add_u32 s26, s26, s8
	ds_read_b128 v[58:61], v237 offset:16384
	ds_read_b128 v[62:65], v237 offset:17408
	ds_read_b128 v[50:53], v237 offset:18432
	ds_read_b128 v[54:57], v237 offset:19456
	ds_read_b128 v[42:45], v237 offset:20480
	ds_read_b128 v[46:49], v237 offset:21504
	ds_read_b128 v[34:37], v237 offset:22528
	ds_read_b128 v[38:41], v237 offset:23552
	global_load_lds_dwordx4 v[224:225], off
	s_mov_b32 m0, s46
	s_addc_u32 s27, s27, s9
	global_load_lds_dwordx4 v[222:223], off
	v_lshl_add_u64 v[232:233], s[26:27], 0, v[200:201]
	s_mov_b32 m0, s47
	v_lshl_add_u64 v[230:231], s[26:27], 0, v[202:203]
	global_load_lds_dwordx4 v[232:233], off
	s_mov_b32 m0, s48
	v_lshl_add_u64 v[226:227], v[68:69], 0, v[204:205]
	global_load_lds_dwordx4 v[230:231], off
	s_mov_b32 m0, s33
	v_lshl_add_u64 v[228:229], v[68:69], 0, v[206:207]
	global_load_lds_dwordx4 v[226:227], off
	s_mov_b32 m0, s34
	s_and_b64 vcc, exec, s[2:3]
	global_load_lds_dwordx4 v[228:229], off
	s_waitcnt vmcnt(8)
	s_waitcnt lgkmcnt(0)
	s_barrier
	s_cbranch_vccnz .LBB0_1387
	s_nop 4
	s_waitcnt lgkmcnt(0)
	v_mfma_f32_16x16x128_f8f6f4 v[134:137], v[18:25], v[58:65], v[134:137]
	v_mfma_f32_16x16x128_f8f6f4 v[130:133], v[26:33], v[58:65], v[130:133]
	v_mfma_f32_16x16x128_f8f6f4 v[118:121], v[18:25], v[50:57], v[118:121]
	v_mfma_f32_16x16x128_f8f6f4 v[110:113], v[26:33], v[50:57], v[110:113]
	v_mfma_f32_16x16x128_f8f6f4 v[102:105], v[18:25], v[42:49], v[102:105]
	v_mfma_f32_16x16x128_f8f6f4 v[94:97], v[26:33], v[42:49], v[94:97]
	v_mfma_f32_16x16x128_f8f6f4 v[86:89], v[18:25], v[34:41], v[86:89]
	v_mfma_f32_16x16x128_f8f6f4 v[78:81], v[26:33], v[34:41], v[78:81]
	s_nop 4
	v_mfma_f32_16x16x128_f8f6f4 v[126:129], v[2:9], v[58:65], v[126:129]
	v_mfma_f32_16x16x128_f8f6f4 v[114:117], v[10:17], v[58:65], v[114:117]
	v_mfma_f32_16x16x128_f8f6f4 v[106:109], v[2:9], v[50:57], v[106:109]
	v_mfma_f32_16x16x128_f8f6f4 v[98:101], v[10:17], v[50:57], v[98:101]
	v_mfma_f32_16x16x128_f8f6f4 v[90:93], v[2:9], v[42:49], v[90:93]
	v_mfma_f32_16x16x128_f8f6f4 v[82:85], v[10:17], v[42:49], v[82:85]
	v_mfma_f32_16x16x128_f8f6f4 v[74:77], v[2:9], v[34:41], v[74:77]
	v_mfma_f32_16x16x128_f8f6f4 v[70:73], v[10:17], v[34:41], v[70:73]
; #define PG8_STAGE(bufoff, gbase, v0, v1) do { \
;         __builtin_amdgcn_global_load_lds((const unsigned*)((const char*)(gbase) + (v0)), (LAS unsigned*)(lds + (bufoff) + ldsw), 16, 0, 0); \
;         __builtin_amdgcn_global_load_lds((const unsigned*)((const char*)(gbase) + (v1)), (LAS unsigned*)(lds + (bufoff) + ldsw + 8192), 16, 0, 0); } while (0)
; #define PG8_LDA(dst, b, h) do { _Pragma("unroll") for (int m = 0; m < 4; ++m) { const v4i lo_ = *(const LAS v4i*)(lds + PG8_SA(b, h) + aoff + m * 2048), hi_ = *(const LAS v4i*)(lds + PG8_SA(b, h) + aoff + m * 2048 + 1024); \
;         dst[m] = __builtin_shufflevector(lo_, hi_, 0, 1, 2, 3, 4, 5, 6, 7); } } while (0)
; #define PG8_LDB(dst, b, h) do { _Pragma("unroll") for (int n = 0; n < 2; ++n) { const v4i lo_ = *(const LAS v4i*)(lds + PG8_SB(b, h) + boff + n * 2048), hi_ = *(const LAS v4i*)(lds + PG8_SB(b, h) + boff + n * 2048 + 1024); \
;         dst[n] = __builtin_shufflevector(lo_, hi_, 0, 1, 2, 3, 4, 5, 6, 7); } } while (0)
; #define PG8_WAIT_V(n) asm volatile("s_waitcnt vmcnt(" #n ")" ::: "memory")
; #define PG8_WAIT_L(n) asm volatile("s_waitcnt lgkmcnt(" #n ")" ::: "memory")
; #define PG8_BAR __builtin_amdgcn_s_barrier()
; #define PG8_SCHED __builtin_amdgcn_sched_barrier(0)
; template <class Epi, class Sched, bool FP8 = false>
; __device__ __forceinline__ void gemm_phase(LAS unsigned char* lds, const int K, const Sched& S, const Epi& E) {
;     ...
;             PG8_LDB(B0, 1, 0); PG8_LDB(B1, 1, 1); PG8_SCHED; PG8_LDA(At, 1, 0); PG8_STAGE(PG8_SA(0, 1), a2, x2, x3);
;             PG8_WAIT_V(8); PG8_WAIT_L(0); PG8_BAR; PG8_MMA(0, 0, At, B0); PG8_MMA(0, 1, At, B1); PG8_BAR; PG8_SCHED;
;             PG8_LDA(At, 1, 1); PG8_STAGE(PG8_SB(1, 0), b3, voffB[0], voffB[1]); PG8_STAGE(PG8_SB(1, 1), b3 + hstepB, voffB[0], voffB[1]); PG8_STAGE(PG8_SA(1, 0), a3, x0, x1);
;             PG8_WAIT_V(8); PG8_WAIT_L(0); PG8_BAR; if (!lo_only) { PG8_MMA(1, 0, At, B0); PG8_MMA(1, 1, At, B1); } PG8_BAR; PG8_SCHED;
;         }
.LBB0_1387:
	s_barrier
	v_add_u32_e32 v2, s49, v199
	v_add_u32_e32 v14, s52, v199
	ds_read_b128 v[18:21], v2
	ds_read_b128 v[22:25], v2 offset:1024
	ds_read_b128 v[26:29], v2 offset:2048
	ds_read_b128 v[30:33], v2 offset:3072
	ds_read_b128 v[2:5], v14
	ds_read_b128 v[6:9], v14 offset:1024
	ds_read_b128 v[10:13], v14 offset:2048
	ds_read_b128 v[14:17], v14 offset:3072
	s_mov_b32 m0, s35
	v_lshl_add_u64 v[240:241], v[68:69], 0, v[208:209]
	s_waitcnt lgkmcnt(0)
	ds_read_b128 v[34:37], v237 offset:32768
	ds_read_b128 v[38:41], v237 offset:33792
	ds_read_b128 v[42:45], v237 offset:34816
	ds_read_b128 v[46:49], v237 offset:35840
	ds_read_b128 v[50:53], v237 offset:36864
	ds_read_b128 v[54:57], v237 offset:37888
	ds_read_b128 v[58:61], v237 offset:38912
	ds_read_b128 v[62:65], v237 offset:39936
	global_load_lds_dwordx4 v[240:241], off
	v_lshl_add_u64 v[68:69], v[68:69], 0, v[210:211]
	s_mov_b32 m0, s36
	s_nop 0
	global_load_lds_dwordx4 v[68:69], off
	s_waitcnt vmcnt(8)
	s_waitcnt lgkmcnt(0)
	s_barrier
	s_nop 4
	s_waitcnt lgkmcnt(0)
	v_mfma_f32_16x16x128_f8f6f4 v[194:197], v[18:25], v[34:41], v[194:197]
	v_mfma_f32_16x16x128_f8f6f4 v[190:193], v[26:33], v[34:41], v[190:193]
	v_mfma_f32_16x16x128_f8f6f4 v[186:189], v[18:25], v[42:49], v[186:189]
	v_mfma_f32_16x16x128_f8f6f4 v[182:185], v[26:33], v[42:49], v[182:185]
	v_mfma_f32_16x16x128_f8f6f4 v[174:177], v[18:25], v[50:57], v[174:177]
	v_mfma_f32_16x16x128_f8f6f4 v[166:169], v[26:33], v[50:57], v[166:169]
	v_mfma_f32_16x16x128_f8f6f4 v[158:161], v[18:25], v[58:65], v[158:161]
	v_mfma_f32_16x16x128_f8f6f4 v[150:153], v[26:33], v[58:65], v[150:153]
	s_nop 4
	v_mfma_f32_16x16x128_f8f6f4 v[178:181], v[2:9], v[34:41], v[178:181]
	v_mfma_f32_16x16x128_f8f6f4 v[170:173], v[10:17], v[34:41], v[170:173]
	v_mfma_f32_16x16x128_f8f6f4 v[162:165], v[2:9], v[42:49], v[162:165]
	v_mfma_f32_16x16x128_f8f6f4 v[154:157], v[10:17], v[42:49], v[154:157]
	v_mfma_f32_16x16x128_f8f6f4 v[146:149], v[2:9], v[50:57], v[146:149]
	v_mfma_f32_16x16x128_f8f6f4 v[142:145], v[10:17], v[50:57], v[142:145]
	v_mfma_f32_16x16x128_f8f6f4 v[138:141], v[2:9], v[58:65], v[138:141]
	v_mfma_f32_16x16x128_f8f6f4 v[122:125], v[10:17], v[58:65], v[122:125]
	s_barrier
	s_add_i32 s26, s49, s31
	v_lshl_add_u64 v[68:69], v[224:225], 0, s[14:15]
	s_mov_b32 m0, s26
	ds_read_b128 v[58:61], v237 offset:49152
	ds_read_b128 v[62:65], v237 offset:50176
	ds_read_b128 v[50:53], v237 offset:51200
	ds_read_b128 v[54:57], v237 offset:52224
	ds_read_b128 v[42:45], v237 offset:53248
	ds_read_b128 v[46:49], v237 offset:54272
	ds_read_b128 v[34:37], v237 offset:55296
	ds_read_b128 v[38:41], v237 offset:56320
	global_load_lds_dwordx4 v[68:69], off
	v_lshl_add_u64 v[68:69], v[222:223], 0, s[14:15]
	s_add_i32 m0, s26, 0x2000
	s_add_i32 s26, s52, s31
	global_load_lds_dwordx4 v[68:69], off
	v_lshl_add_u64 v[68:69], v[232:233], 0, s[14:15]
	s_mov_b32 m0, s26
	s_and_b64 vcc, exec, s[2:3]
	global_load_lds_dwordx4 v[68:69], off
	v_lshl_add_u64 v[68:69], v[230:231], 0, s[14:15]
	s_add_i32 m0, s26, 0x2000
	s_nop 0
	global_load_lds_dwordx4 v[68:69], off
	v_lshl_add_u64 v[68:69], v[226:227], 0, s[14:15]
	s_mov_b32 m0, s38
	s_nop 0
	global_load_lds_dwordx4 v[68:69], off
	v_lshl_add_u64 v[68:69], v[228:229], 0, s[14:15]
	s_mov_b32 m0, s39
	s_nop 0
	global_load_lds_dwordx4 v[68:69], off
	s_waitcnt vmcnt(8)
	s_waitcnt lgkmcnt(0)
	s_barrier
	s_cbranch_vccnz .LBB0_1384
	s_nop 4
	s_waitcnt lgkmcnt(0)
	v_mfma_f32_16x16x128_f8f6f4 v[134:137], v[18:25], v[58:65], v[134:137]
	v_mfma_f32_16x16x128_f8f6f4 v[130:133], v[26:33], v[58:65], v[130:133]
	v_mfma_f32_16x16x128_f8f6f4 v[118:121], v[18:25], v[50:57], v[118:121]
	v_mfma_f32_16x16x128_f8f6f4 v[110:113], v[26:33], v[50:57], v[110:113]
	v_mfma_f32_16x16x128_f8f6f4 v[102:105], v[18:25], v[42:49], v[102:105]
	v_mfma_f32_16x16x128_f8f6f4 v[94:97], v[26:33], v[42:49], v[94:97]
	v_mfma_f32_16x16x128_f8f6f4 v[86:89], v[18:25], v[34:41], v[86:89]
	v_mfma_f32_16x16x128_f8f6f4 v[78:81], v[26:33], v[34:41], v[78:81]
	s_nop 4
	v_mfma_f32_16x16x128_f8f6f4 v[126:129], v[2:9], v[58:65], v[126:129]
	v_mfma_f32_16x16x128_f8f6f4 v[114:117], v[10:17], v[58:65], v[114:117]
	v_mfma_f32_16x16x128_f8f6f4 v[106:109], v[2:9], v[50:57], v[106:109]
	v_mfma_f32_16x16x128_f8f6f4 v[98:101], v[10:17], v[50:57], v[98:101]
	v_mfma_f32_16x16x128_f8f6f4 v[90:93], v[2:9], v[42:49], v[90:93]
	v_mfma_f32_16x16x128_f8f6f4 v[82:85], v[10:17], v[42:49], v[82:85]
	v_mfma_f32_16x16x128_f8f6f4 v[74:77], v[2:9], v[34:41], v[74:77]
	v_mfma_f32_16x16x128_f8f6f4 v[70:73], v[10:17], v[34:41], v[70:73]
	s_branch .LBB0_1384

; #define LAS __attribute__((address_space(3)))
; __device__ __forceinline__ void phase10(const Args& a, LAS unsigned char* lds, int lane, int wave, int vcu, int G) {
;     unsigned char* ws = a.ws;
;     const float* mod = (const float*)(ws + WS_MOD); const unsigned char* SO = ws + WS_SLOTOUT; const int* tokslot = (const int*)(ws + T_TOKSLOT); const float* gp = a.in[9];
;     LAS float* ysc = (LAS float*)(lds + wave * 8192);
;     const unsigned lo16_ = 16u * (unsigned)lane;
;     int nslot = tokslot[(size_t)(vcu * 8 + wave) * 8 + (lane & 7)];
; #pragma unroll 1
;     for (int t = vcu * 8 + wave; t < NT; t += G * 8) {
;         const float* mr = mod + (size_t)(t >> 11) * 12288;
;         const int myslot = lane < 8 ? nslot : SH_ROW0 + t;
;         { const int tn = t + G * 8 < NT ? t + G * 8 : t; nslot = tokslot[(size_t)tn * 8 + (lane & 7)]; }
.LBB0_1462:
	s_setprio 0
	s_cmp_gt_i32 s94, 11
	s_cselect_b64 s[0:1], -1, 0
	s_cmp_lt_i32 s95, 12
	s_cselect_b64 s[2:3], -1, 0
	s_or_b64 s[0:1], s[0:1], s[2:3]
	s_and_b64 vcc, exec, s[0:1]
	s_cbranch_vccnz .LBB0_1466
	s_lshl_b32 s4, s71, 3
	v_readfirstlane_b32 s0, v0
	s_ashr_i32 s3, s0, 6
	s_add_i32 s14, s3, s4
	s_cmpk_gt_i32 s14, 0x3fff
	s_cbranch_scc1 .LBB0_1466
	s_add_u32 s16, s92, 0x9e00000
	s_addc_u32 s17, s93, 0
	s_add_u32 s0, s92, 0x39cb0000
	s_addc_u32 s1, s93, 0
	s_ashr_i32 s15, s14, 31
	s_lshl_b64 s[6:7], s[14:15], 5
	v_and_b32_e32 v1, 7, v0
	s_add_u32 s6, s0, s6
	v_lshlrev_b32_e32 v32, 2, v1
	s_addc_u32 s7, s1, s7
	s_waitcnt lgkmcnt(0)
	global_load_dword v55, v32, s[6:7]
	v_mov_b32_e32 v33, 0
	v_lshl_add_u64 v[34:35], s[0:1], 0, v[32:33]
	s_lshl_b32 s0, s3, 13
	s_add_i32 s12, s0, 0
	s_lshl_b32 s2, s97, 3
	s_ashr_i32 s5, s3, 31
	s_ashr_i32 s6, s4, 31
	s_add_u32 s8, s3, s4
	s_addc_u32 s9, s5, s6
	s_lshl_b64 s[4:5], s[8:9], 12
	s_add_u32 s3, s92, s4
	s_addc_u32 s5, s93, s5
	s_add_u32 s4, s3, 0x26200e00
	s_addc_u32 s5, s5, 0
	s_ashr_i32 s3, s2, 31
	v_and_b32_e32 v0, 63, v0
	s_lshl_b64 s[6:7], s[2:3], 12
	s_lshl_b64 s[8:9], s[8:9], 13
	v_lshlrev_b32_e32 v54, 4, v0
	v_cmp_gt_u32_e64 s[0:1], 8, v0
	v_lshlrev_b32_e32 v0, 6, v0
	s_add_u32 s8, s90, s8
	v_readlane_b32 s40, v246, 3
	s_addc_u32 s9, s91, s9
	s_lshl_b64 s[10:11], s[2:3], 13
	v_mov_b32_e32 v32, 0x3a8637bd
	v_mov_b32_e32 v56, 0x3a000000
	s_mov_b32 s3, 0x800000
	v_add_u32_e32 v57, s12, v0
	v_add_u32_e32 v58, s12, v54
	v_readlane_b32 s42, v246, 5
	v_readlane_b32 s43, v246, 6
	v_readlane_b32 s41, v246, 4
	v_readlane_b32 s44, v246, 7
	v_readlane_b32 s45, v246, 8
	v_readlane_b32 s46, v246, 9
	v_readlane_b32 s47, v246, 10
	v_readlane_b32 s48, v246, 11
	v_readlane_b32 s49, v246, 12
	v_readlane_b32 s50, v246, 13
	v_readlane_b32 s51, v246, 14
	v_readlane_b32 s52, v246, 15
	v_readlane_b32 s53, v246, 16
	v_readlane_b32 s54, v246, 17
	v_readlane_b32 s55, v246, 18
